# plan N: in-proj-0 with 29 conversion WGs (7 GEMM rounds on 227 WGs), out-proj-0 (64 WGs) and in-proj-1 (44 WGs) take the moved gate/up experts; hand-written conversion routine in all three
# baseline (speedup 1.0000x reference)
.LBB0_254:
	s_load_dwordx4 s[0:3], s[8:9], 0x138
	s_waitcnt lgkmcnt(0)
	s_mov_b64 s[4:5], s[0:1]
	s_cmp_lt_i32 s4, 3
	s_cselect_b64 s[0:1], -1, 0
	s_cmp_gt_i32 s5, 2
	s_cselect_b64 s[2:3], -1, 0
	s_and_b64 s[0:1], s[0:1], s[2:3]
	s_andn2_b64 vcc, exec, s[0:1]
	s_cbranch_vccnz .LBB0_356
	s_mov_b64 s[0:1], s[8:9]
	v_mbcnt_lo_u32_b32 v152, -1, 0
	v_mbcnt_hi_u32_b32 v152, -1, v152
	s_load_dword s38, s[8:9], 0x148
	s_add_u32 s2, s8, 0x148
	v_readlane_b32 s4, v243, 0
	s_addc_u32 s3, s9, 0
	v_readlane_b32 s5, v243, 1
	s_waitcnt lgkmcnt(0)
	s_sub_i32 s39, s38, 29
	s_cmp_lt_i32 s4, s39
	s_mov_b64 s[4:5], -1
	s_cbranch_scc1 .LBB0_276
	v_readlane_b32 s4, v243, 0
	s_sub_i32 s4, s4, s39
	s_lshl_b32 s4, s4, 3
	s_add_i32 s19, s4, s94
	s_mov_b32 s4, s19
	s_mov_b32 s5, 0xe8
	s_mov_b32 s6, 0x2200
	s_waitcnt vmcnt(0)
	s_cmp_ge_u32 s4, s6
	s_cbranch_scc1 .Lp2c0_done
	v_readlane_b32 s8, v243, 7
	v_readlane_b32 s9, v243, 8
	s_load_dwordx2 s[10:11], s[8:9], 0x130
	s_load_dwordx2 s[12:13], s[8:9], 0xf8
	s_load_dwordx2 s[14:15], s[8:9], 0x108
	v_mbcnt_lo_u32_b32 v142, -1, 0
	v_mbcnt_hi_u32_b32 v142, -1, v142
	v_lshrrev_b32_e32 v143, 3, v142
	v_and_b32_e32 v142, 7, v142
	v_lshlrev_b32_e32 v136, 16, v143
	v_lshl_add_u32 v136, v142, 4, v136
	v_add_u32_e32 v137, 0x1000, v136
	v_add_u32_e32 v138, 0x2000, v136
	v_add_u32_e32 v139, 0x3000, v136
	v_lshlrev_b32_e32 v140, 12, v142
	v_lshl_add_u32 v140, v143, 4, v140
	v_mov_b32_e32 v141, 0x43e00000
	s_mov_b32 s28, 0xc3e00000
	s_waitcnt lgkmcnt(0)
	s_add_u32 s10, s10, 0x2900000
	s_addc_u32 s11, s11, 0
	s_lshr_b32 s22, s4, 8
	s_and_b32 s23, s4, 0xff
	s_and_b32 s27, s22, 1
	s_lshr_b32 s22, s22, 1
	s_cmp_eq_u32 s27, 0
	s_cselect_b64 s[16:17], s[12:13], s[14:15]
	s_add_i32 s22, s22, 20
	s_lshl_b32 s24, s22, 22
	s_lshr_b32 s25, s23, 5
	s_lshl_b32 s25, s25, 19
	s_and_b32 s26, s23, 31
	s_lshl_b32 s26, s26, 7
	s_add_i32 s24, s24, s25
	s_add_i32 s24, s24, s26
	s_add_u32 s16, s16, s24
	s_addc_u32 s17, s17, 0
	s_nop 0
	global_load_dwordx4 v[0:3], v136, s[16:17] nt
	global_load_dwordx4 v[4:7], v137, s[16:17] nt
	global_load_dwordx4 v[8:11], v138, s[16:17] nt
	global_load_dwordx4 v[12:15], v139, s[16:17] nt
	s_add_u32 s16, s16, 0x4000
	s_addc_u32 s17, s17, 0
	s_nop 0
	global_load_dwordx4 v[16:19], v136, s[16:17] nt
	global_load_dwordx4 v[20:23], v137, s[16:17] nt
	global_load_dwordx4 v[24:27], v138, s[16:17] nt
	global_load_dwordx4 v[28:31], v139, s[16:17] nt
	s_add_u32 s16, s16, 0x4000
	s_addc_u32 s17, s17, 0
	s_nop 0
	global_load_dwordx4 v[32:35], v136, s[16:17] nt
	global_load_dwordx4 v[36:39], v137, s[16:17] nt
	global_load_dwordx4 v[40:43], v138, s[16:17] nt
	global_load_dwordx4 v[44:47], v139, s[16:17] nt
	s_add_u32 s16, s16, 0x4000
	s_addc_u32 s17, s17, 0
	s_nop 0
	global_load_dwordx4 v[48:51], v136, s[16:17] nt
	global_load_dwordx4 v[52:55], v137, s[16:17] nt
	global_load_dwordx4 v[56:59], v138, s[16:17] nt
	global_load_dwordx4 v[60:63], v139, s[16:17] nt
	s_add_i32 s7, s4, s5
	s_cmp_lt_u32 s7, s6
	s_cbranch_scc0 .Lp2c0_p_last
	s_lshr_b32 s22, s7, 8
	s_and_b32 s23, s7, 0xff
	s_and_b32 s27, s22, 1
	s_lshr_b32 s22, s22, 1
	s_cmp_eq_u32 s27, 0
	s_cselect_b64 s[16:17], s[12:13], s[14:15]
	s_add_i32 s22, s22, 20
	s_lshl_b32 s24, s22, 22
	s_lshr_b32 s25, s23, 5
	s_lshl_b32 s25, s25, 19
	s_and_b32 s26, s23, 31
	s_lshl_b32 s26, s26, 7
	s_add_i32 s24, s24, s25
	s_add_i32 s24, s24, s26
	s_add_u32 s16, s16, s24
	s_addc_u32 s17, s17, 0
	s_nop 0
	global_load_dwordx4 v[64:67], v136, s[16:17] nt
	global_load_dwordx4 v[68:71], v137, s[16:17] nt
	global_load_dwordx4 v[72:75], v138, s[16:17] nt
	global_load_dwordx4 v[76:79], v139, s[16:17] nt
	s_add_u32 s16, s16, 0x4000
	s_addc_u32 s17, s17, 0
	s_nop 0
	global_load_dwordx4 v[80:83], v136, s[16:17] nt
	global_load_dwordx4 v[84:87], v137, s[16:17] nt
	global_load_dwordx4 v[88:91], v138, s[16:17] nt
	global_load_dwordx4 v[92:95], v139, s[16:17] nt
	s_add_u32 s16, s16, 0x4000
	s_addc_u32 s17, s17, 0
	s_nop 0
	global_load_dwordx4 v[96:99], v136, s[16:17] nt
	global_load_dwordx4 v[100:103], v137, s[16:17] nt
	global_load_dwordx4 v[104:107], v138, s[16:17] nt
	global_load_dwordx4 v[108:111], v139, s[16:17] nt
	s_add_u32 s16, s16, 0x4000
	s_addc_u32 s17, s17, 0
	s_nop 0
	global_load_dwordx4 v[112:115], v136, s[16:17] nt
	global_load_dwordx4 v[116:119], v137, s[16:17] nt
	global_load_dwordx4 v[120:123], v138, s[16:17] nt
	global_load_dwordx4 v[124:127], v139, s[16:17] nt
	s_waitcnt vmcnt(16)
	s_branch .Lp2c0_p_st

.Lp4c0_done:
	s_mov_b32 s4, s19
	s_mov_b32 s5, 0x200
	s_mov_b32 s6, 0x600
	s_waitcnt vmcnt(0)
	s_cmp_ge_u32 s4, s6
	s_cbranch_scc1 .Lp4c1_done
	v_readlane_b32 s8, v243, 7
	v_readlane_b32 s9, v243, 8
	s_load_dwordx2 s[10:11], s[8:9], 0x130
	s_load_dwordx2 s[12:13], s[8:9], 0xf8
	s_load_dwordx2 s[14:15], s[8:9], 0x108
	v_mbcnt_lo_u32_b32 v172, -1, 0
	v_mbcnt_hi_u32_b32 v172, -1, v172
	v_lshrrev_b32_e32 v173, 3, v172
	v_and_b32_e32 v172, 7, v172
	v_lshlrev_b32_e32 v166, 16, v173
	v_lshl_add_u32 v166, v172, 4, v166
	v_add_u32_e32 v167, 0x1000, v166
	v_add_u32_e32 v168, 0x2000, v166
	v_add_u32_e32 v169, 0x3000, v166
	v_lshlrev_b32_e32 v170, 12, v172
	v_lshl_add_u32 v170, v173, 4, v170
	v_mov_b32_e32 v171, 0x43e00000
	s_mov_b32 s28, 0xc3e00000
	s_waitcnt lgkmcnt(0)
	s_add_u32 s10, s10, 0x2900000
	s_addc_u32 s11, s11, 0
	s_lshr_b32 s22, s4, 8
	s_and_b32 s23, s4, 0xff
	s_and_b32 s27, s22, 1
	s_lshr_b32 s22, s22, 1
	s_cmp_eq_u32 s27, 0
	s_cselect_b64 s[16:17], s[12:13], s[14:15]
	s_add_i32 s22, s22, 37
	s_lshl_b32 s24, s22, 22
	s_lshr_b32 s25, s23, 5
	s_lshl_b32 s25, s25, 19
	s_and_b32 s26, s23, 31
	s_lshl_b32 s26, s26, 7
	s_add_i32 s24, s24, s25
	s_add_i32 s24, s24, s26
	s_add_u32 s16, s16, s24
	s_addc_u32 s17, s17, 0
	s_nop 0
	global_load_dwordx4 v[0:3], v166, s[16:17] nt
	global_load_dwordx4 v[4:7], v167, s[16:17] nt
	global_load_dwordx4 v[8:11], v168, s[16:17] nt
	global_load_dwordx4 v[12:15], v169, s[16:17] nt
	s_add_u32 s16, s16, 0x4000
	s_addc_u32 s17, s17, 0
	s_nop 0
	global_load_dwordx4 v[16:19], v166, s[16:17] nt
	global_load_dwordx4 v[20:23], v167, s[16:17] nt
	global_load_dwordx4 v[24:27], v168, s[16:17] nt
	global_load_dwordx4 v[28:31], v169, s[16:17] nt
	s_add_u32 s16, s16, 0x4000
	s_addc_u32 s17, s17, 0
	s_nop 0
	global_load_dwordx4 v[32:35], v166, s[16:17] nt
	global_load_dwordx4 v[36:39], v167, s[16:17] nt
	global_load_dwordx4 v[40:43], v168, s[16:17] nt
	global_load_dwordx4 v[44:47], v169, s[16:17] nt
	s_add_u32 s16, s16, 0x4000
	s_addc_u32 s17, s17, 0
	s_nop 0
	global_load_dwordx4 v[48:51], v166, s[16:17] nt
	global_load_dwordx4 v[52:55], v167, s[16:17] nt
	global_load_dwordx4 v[56:59], v168, s[16:17] nt
	global_load_dwordx4 v[60:63], v169, s[16:17] nt
	s_add_i32 s7, s4, s5
	s_cmp_lt_u32 s7, s6
	s_cbranch_scc0 .Lp4c1_p_last
	s_lshr_b32 s22, s7, 8
	s_and_b32 s23, s7, 0xff
	s_and_b32 s27, s22, 1
	s_lshr_b32 s22, s22, 1
	s_cmp_eq_u32 s27, 0
	s_cselect_b64 s[16:17], s[12:13], s[14:15]
	s_add_i32 s22, s22, 37
	s_lshl_b32 s24, s22, 22
	s_lshr_b32 s25, s23, 5
	s_lshl_b32 s25, s25, 19
	s_and_b32 s26, s23, 31
	s_lshl_b32 s26, s26, 7
	s_add_i32 s24, s24, s25
	s_add_i32 s24, s24, s26
	s_add_u32 s16, s16, s24
	s_addc_u32 s17, s17, 0
	s_nop 0
	global_load_dwordx4 v[64:67], v166, s[16:17] nt
	global_load_dwordx4 v[68:71], v167, s[16:17] nt
	global_load_dwordx4 v[72:75], v168, s[16:17] nt
	global_load_dwordx4 v[76:79], v169, s[16:17] nt
	s_add_u32 s16, s16, 0x4000
	s_addc_u32 s17, s17, 0
	s_nop 0
	global_load_dwordx4 v[80:83], v166, s[16:17] nt
	global_load_dwordx4 v[84:87], v167, s[16:17] nt
	global_load_dwordx4 v[88:91], v168, s[16:17] nt
	global_load_dwordx4 v[92:95], v169, s[16:17] nt
	s_add_u32 s16, s16, 0x4000
	s_addc_u32 s17, s17, 0
	s_nop 0
	global_load_dwordx4 v[96:99], v166, s[16:17] nt
	global_load_dwordx4 v[100:103], v167, s[16:17] nt
	global_load_dwordx4 v[104:107], v168, s[16:17] nt
	global_load_dwordx4 v[108:111], v169, s[16:17] nt
	s_add_u32 s16, s16, 0x4000
	s_addc_u32 s17, s17, 0
	s_nop 0
	global_load_dwordx4 v[112:115], v166, s[16:17] nt
	global_load_dwordx4 v[116:119], v167, s[16:17] nt
	global_load_dwordx4 v[120:123], v168, s[16:17] nt
	global_load_dwordx4 v[124:127], v169, s[16:17] nt
	s_waitcnt vmcnt(16)
	s_branch .Lp4c1_p_st

.Lp4c1_p_st:
	s_lshr_b32 s22, s4, 8
	s_and_b32 s23, s4, 0xff
	s_and_b32 s27, s22, 1
	s_lshr_b32 s22, s22, 1
	s_add_i32 s22, s22, 37
	s_mul_i32 s24, s22, 0x300000
	s_lshr_b32 s25, s23, 5
	s_lshl_b32 s25, s25, 7
	s_add_i32 s24, s24, s25
	s_and_b32 s26, s23, 31
	s_lshr_b32 s25, s26, 2
	s_lshl_b32 s25, s25, 18
	s_add_i32 s24, s24, s25
	s_lshl_b32 s25, s27, 17
	s_add_i32 s24, s24, s25
	s_and_b32 s25, s26, 3
	s_lshl_b32 s25, s25, 15
	s_add_i32 s24, s24, s25
	s_add_u32 s20, s10, s24
	s_addc_u32 s21, s11, 0
	v_mul_f32_e32 v0, 0x42000000, v0
	v_mul_f32_e32 v4, 0x42000000, v4
	v_mul_f32_e32 v8, 0x42000000, v8
	v_mul_f32_e32 v12, 0x42000000, v12
	v_mul_f32_e32 v16, 0x42000000, v16
	v_mul_f32_e32 v20, 0x42000000, v20
	v_mul_f32_e32 v24, 0x42000000, v24
	v_mul_f32_e32 v28, 0x42000000, v28
	v_mul_f32_e32 v32, 0x42000000, v32
	v_mul_f32_e32 v36, 0x42000000, v36
	v_mul_f32_e32 v40, 0x42000000, v40
	v_mul_f32_e32 v44, 0x42000000, v44
	v_mul_f32_e32 v48, 0x42000000, v48
	v_mul_f32_e32 v52, 0x42000000, v52
	v_mul_f32_e32 v56, 0x42000000, v56
	v_mul_f32_e32 v60, 0x42000000, v60
	v_med3_f32 v0, v0, s28, v171
	v_med3_f32 v4, v4, s28, v171
	v_med3_f32 v8, v8, s28, v171
	v_med3_f32 v12, v12, s28, v171
	v_med3_f32 v16, v16, s28, v171
	v_med3_f32 v20, v20, s28, v171
	v_med3_f32 v24, v24, s28, v171
	v_med3_f32 v28, v28, s28, v171
	v_med3_f32 v32, v32, s28, v171
	v_med3_f32 v36, v36, s28, v171
	v_med3_f32 v40, v40, s28, v171
	v_med3_f32 v44, v44, s28, v171
	v_med3_f32 v48, v48, s28, v171
	v_med3_f32 v52, v52, s28, v171
	v_med3_f32 v56, v56, s28, v171
	v_med3_f32 v60, v60, s28, v171
	v_cvt_pk_fp8_f32 v158, v0, v4
	v_cvt_pk_fp8_f32 v159, v16, v20
	v_cvt_pk_fp8_f32 v160, v32, v36
	v_cvt_pk_fp8_f32 v161, v48, v52
	v_cvt_pk_fp8_f32 v158, v8, v12 op_sel:[0,0,1]
	v_cvt_pk_fp8_f32 v159, v24, v28 op_sel:[0,0,1]
	v_cvt_pk_fp8_f32 v160, v40, v44 op_sel:[0,0,1]
	v_cvt_pk_fp8_f32 v161, v56, v60 op_sel:[0,0,1]
	s_nop 0
	global_store_dwordx4 v170, v[158:161], s[20:21]
	v_mul_f32_e32 v1, 0x42000000, v1
	v_mul_f32_e32 v5, 0x42000000, v5
	v_mul_f32_e32 v9, 0x42000000, v9
	v_mul_f32_e32 v13, 0x42000000, v13
	v_mul_f32_e32 v17, 0x42000000, v17
	v_mul_f32_e32 v21, 0x42000000, v21
	v_mul_f32_e32 v25, 0x42000000, v25
	v_mul_f32_e32 v29, 0x42000000, v29
	v_mul_f32_e32 v33, 0x42000000, v33
	v_mul_f32_e32 v37, 0x42000000, v37
	v_mul_f32_e32 v41, 0x42000000, v41
	v_mul_f32_e32 v45, 0x42000000, v45
	v_mul_f32_e32 v49, 0x42000000, v49
	v_mul_f32_e32 v53, 0x42000000, v53
	v_mul_f32_e32 v57, 0x42000000, v57
	v_mul_f32_e32 v61, 0x42000000, v61
	v_med3_f32 v1, v1, s28, v171
	v_med3_f32 v5, v5, s28, v171
	v_med3_f32 v9, v9, s28, v171
	v_med3_f32 v13, v13, s28, v171
	v_med3_f32 v17, v17, s28, v171
	v_med3_f32 v21, v21, s28, v171
	v_med3_f32 v25, v25, s28, v171
	v_med3_f32 v29, v29, s28, v171
	v_med3_f32 v33, v33, s28, v171
	v_med3_f32 v37, v37, s28, v171
	v_med3_f32 v41, v41, s28, v171
	v_med3_f32 v45, v45, s28, v171
	v_med3_f32 v49, v49, s28, v171
	v_med3_f32 v53, v53, s28, v171
	v_med3_f32 v57, v57, s28, v171
	v_med3_f32 v61, v61, s28, v171
	v_cvt_pk_fp8_f32 v162, v1, v5
	v_cvt_pk_fp8_f32 v163, v17, v21
	v_cvt_pk_fp8_f32 v164, v33, v37
	v_cvt_pk_fp8_f32 v165, v49, v53
	v_cvt_pk_fp8_f32 v162, v9, v13 op_sel:[0,0,1]
	v_cvt_pk_fp8_f32 v163, v25, v29 op_sel:[0,0,1]
	v_cvt_pk_fp8_f32 v164, v41, v45 op_sel:[0,0,1]
	v_cvt_pk_fp8_f32 v165, v57, v61 op_sel:[0,0,1]
	s_nop 0
	global_store_dwordx4 v170, v[162:165], s[20:21] offset:1024
	v_mul_f32_e32 v2, 0x42000000, v2
	v_mul_f32_e32 v6, 0x42000000, v6
	v_mul_f32_e32 v10, 0x42000000, v10
	v_mul_f32_e32 v14, 0x42000000, v14
	v_mul_f32_e32 v18, 0x42000000, v18
	v_mul_f32_e32 v22, 0x42000000, v22
	v_mul_f32_e32 v26, 0x42000000, v26
	v_mul_f32_e32 v30, 0x42000000, v30
	v_mul_f32_e32 v34, 0x42000000, v34
	v_mul_f32_e32 v38, 0x42000000, v38
	v_mul_f32_e32 v42, 0x42000000, v42
	v_mul_f32_e32 v46, 0x42000000, v46
	v_mul_f32_e32 v50, 0x42000000, v50
	v_mul_f32_e32 v54, 0x42000000, v54
	v_mul_f32_e32 v58, 0x42000000, v58
	v_mul_f32_e32 v62, 0x42000000, v62
	v_med3_f32 v2, v2, s28, v171
	v_med3_f32 v6, v6, s28, v171
	v_med3_f32 v10, v10, s28, v171
	v_med3_f32 v14, v14, s28, v171
	v_med3_f32 v18, v18, s28, v171
	v_med3_f32 v22, v22, s28, v171
	v_med3_f32 v26, v26, s28, v171
	v_med3_f32 v30, v30, s28, v171
	v_med3_f32 v34, v34, s28, v171
	v_med3_f32 v38, v38, s28, v171
	v_med3_f32 v42, v42, s28, v171
	v_med3_f32 v46, v46, s28, v171
	v_med3_f32 v50, v50, s28, v171
	v_med3_f32 v54, v54, s28, v171
	v_med3_f32 v58, v58, s28, v171
	v_med3_f32 v62, v62, s28, v171
	v_cvt_pk_fp8_f32 v158, v2, v6
	v_cvt_pk_fp8_f32 v159, v18, v22
	v_cvt_pk_fp8_f32 v160, v34, v38
	v_cvt_pk_fp8_f32 v161, v50, v54
	v_cvt_pk_fp8_f32 v158, v10, v14 op_sel:[0,0,1]
	v_cvt_pk_fp8_f32 v159, v26, v30 op_sel:[0,0,1]
	v_cvt_pk_fp8_f32 v160, v42, v46 op_sel:[0,0,1]
	v_cvt_pk_fp8_f32 v161, v58, v62 op_sel:[0,0,1]
	s_nop 0
	global_store_dwordx4 v170, v[158:161], s[20:21] offset:2048
	v_mul_f32_e32 v3, 0x42000000, v3
	v_mul_f32_e32 v7, 0x42000000, v7
	v_mul_f32_e32 v11, 0x42000000, v11
	v_mul_f32_e32 v15, 0x42000000, v15
	v_mul_f32_e32 v19, 0x42000000, v19
	v_mul_f32_e32 v23, 0x42000000, v23
	v_mul_f32_e32 v27, 0x42000000, v27
	v_mul_f32_e32 v31, 0x42000000, v31
	v_mul_f32_e32 v35, 0x42000000, v35
	v_mul_f32_e32 v39, 0x42000000, v39
	v_mul_f32_e32 v43, 0x42000000, v43
	v_mul_f32_e32 v47, 0x42000000, v47
	v_mul_f32_e32 v51, 0x42000000, v51
	v_mul_f32_e32 v55, 0x42000000, v55
	v_mul_f32_e32 v59, 0x42000000, v59
	v_mul_f32_e32 v63, 0x42000000, v63
	v_med3_f32 v3, v3, s28, v171
	v_med3_f32 v7, v7, s28, v171
	v_med3_f32 v11, v11, s28, v171
	v_med3_f32 v15, v15, s28, v171
	v_med3_f32 v19, v19, s28, v171
	v_med3_f32 v23, v23, s28, v171
	v_med3_f32 v27, v27, s28, v171
	v_med3_f32 v31, v31, s28, v171
	v_med3_f32 v35, v35, s28, v171
	v_med3_f32 v39, v39, s28, v171
	v_med3_f32 v43, v43, s28, v171
	v_med3_f32 v47, v47, s28, v171
	v_med3_f32 v51, v51, s28, v171
	v_med3_f32 v55, v55, s28, v171
	v_med3_f32 v59, v59, s28, v171
	v_med3_f32 v63, v63, s28, v171
	v_cvt_pk_fp8_f32 v162, v3, v7
	v_cvt_pk_fp8_f32 v163, v19, v23
	v_cvt_pk_fp8_f32 v164, v35, v39
	v_cvt_pk_fp8_f32 v165, v51, v55
	v_cvt_pk_fp8_f32 v162, v11, v15 op_sel:[0,0,1]
	v_cvt_pk_fp8_f32 v163, v27, v31 op_sel:[0,0,1]
	v_cvt_pk_fp8_f32 v164, v43, v47 op_sel:[0,0,1]
	v_cvt_pk_fp8_f32 v165, v59, v63 op_sel:[0,0,1]
	s_nop 0
	global_store_dwordx4 v170, v[162:165], s[20:21] offset:3072
	s_cmp_ge_u32 s7, s6
	s_cbranch_scc1 .Lp4c1_done
	s_mov_b32 s4, s7
.Lp4c1_loop:
	s_add_i32 s7, s4, s5
	s_cmp_lt_u32 s7, s6
	s_cbranch_scc0 .Lp4c1_B_last
	s_lshr_b32 s22, s7, 8
	s_and_b32 s23, s7, 0xff
	s_and_b32 s27, s22, 1
	s_lshr_b32 s22, s22, 1
	s_cmp_eq_u32 s27, 0
	s_cselect_b64 s[16:17], s[12:13], s[14:15]
	s_add_i32 s22, s22, 37
	s_lshl_b32 s24, s22, 22
	s_lshr_b32 s25, s23, 5
	s_lshl_b32 s25, s25, 19
	s_and_b32 s26, s23, 31
	s_lshl_b32 s26, s26, 7
	s_add_i32 s24, s24, s25
	s_add_i32 s24, s24, s26
	s_add_u32 s16, s16, s24
	s_addc_u32 s17, s17, 0
	s_nop 0
	global_load_dwordx4 v[0:3], v166, s[16:17] nt
	global_load_dwordx4 v[4:7], v167, s[16:17] nt
	global_load_dwordx4 v[8:11], v168, s[16:17] nt
	global_load_dwordx4 v[12:15], v169, s[16:17] nt
	s_add_u32 s16, s16, 0x4000
	s_addc_u32 s17, s17, 0
	s_nop 0
	global_load_dwordx4 v[16:19], v166, s[16:17] nt
	global_load_dwordx4 v[20:23], v167, s[16:17] nt
	global_load_dwordx4 v[24:27], v168, s[16:17] nt
	global_load_dwordx4 v[28:31], v169, s[16:17] nt
	s_add_u32 s16, s16, 0x4000
	s_addc_u32 s17, s17, 0
	s_nop 0
	global_load_dwordx4 v[32:35], v166, s[16:17] nt
	global_load_dwordx4 v[36:39], v167, s[16:17] nt
	global_load_dwordx4 v[40:43], v168, s[16:17] nt
	global_load_dwordx4 v[44:47], v169, s[16:17] nt
	s_add_u32 s16, s16, 0x4000
	s_addc_u32 s17, s17, 0
	s_nop 0
	global_load_dwordx4 v[48:51], v166, s[16:17] nt
	global_load_dwordx4 v[52:55], v167, s[16:17] nt
	global_load_dwordx4 v[56:59], v168, s[16:17] nt
	global_load_dwordx4 v[60:63], v169, s[16:17] nt
	s_waitcnt vmcnt(20)
	s_branch .Lp4c1_B_st

.Lp4c1_B_st:
	s_lshr_b32 s22, s4, 8
	s_and_b32 s23, s4, 0xff
	s_and_b32 s27, s22, 1
	s_lshr_b32 s22, s22, 1
	s_add_i32 s22, s22, 37
	s_mul_i32 s24, s22, 0x300000
	s_lshr_b32 s25, s23, 5
	s_lshl_b32 s25, s25, 7
	s_add_i32 s24, s24, s25
	s_and_b32 s26, s23, 31
	s_lshr_b32 s25, s26, 2
	s_lshl_b32 s25, s25, 18
	s_add_i32 s24, s24, s25
	s_lshl_b32 s25, s27, 17
	s_add_i32 s24, s24, s25
	s_and_b32 s25, s26, 3
	s_lshl_b32 s25, s25, 15
	s_add_i32 s24, s24, s25
	s_add_u32 s20, s10, s24
	s_addc_u32 s21, s11, 0
	v_mul_f32_e32 v64, 0x42000000, v64
	v_mul_f32_e32 v68, 0x42000000, v68
	v_mul_f32_e32 v72, 0x42000000, v72
	v_mul_f32_e32 v76, 0x42000000, v76
	v_mul_f32_e32 v80, 0x42000000, v80
	v_mul_f32_e32 v84, 0x42000000, v84
	v_mul_f32_e32 v88, 0x42000000, v88
	v_mul_f32_e32 v92, 0x42000000, v92
	v_mul_f32_e32 v96, 0x42000000, v96
	v_mul_f32_e32 v100, 0x42000000, v100
	v_mul_f32_e32 v104, 0x42000000, v104
	v_mul_f32_e32 v108, 0x42000000, v108
	v_mul_f32_e32 v112, 0x42000000, v112
	v_mul_f32_e32 v116, 0x42000000, v116
	v_mul_f32_e32 v120, 0x42000000, v120
	v_mul_f32_e32 v124, 0x42000000, v124
	v_med3_f32 v64, v64, s28, v171
	v_med3_f32 v68, v68, s28, v171
	v_med3_f32 v72, v72, s28, v171
	v_med3_f32 v76, v76, s28, v171
	v_med3_f32 v80, v80, s28, v171
	v_med3_f32 v84, v84, s28, v171
	v_med3_f32 v88, v88, s28, v171
	v_med3_f32 v92, v92, s28, v171
	v_med3_f32 v96, v96, s28, v171
	v_med3_f32 v100, v100, s28, v171
	v_med3_f32 v104, v104, s28, v171
	v_med3_f32 v108, v108, s28, v171
	v_med3_f32 v112, v112, s28, v171
	v_med3_f32 v116, v116, s28, v171
	v_med3_f32 v120, v120, s28, v171
	v_med3_f32 v124, v124, s28, v171
	v_cvt_pk_fp8_f32 v158, v64, v68
	v_cvt_pk_fp8_f32 v159, v80, v84
	v_cvt_pk_fp8_f32 v160, v96, v100
	v_cvt_pk_fp8_f32 v161, v112, v116
	v_cvt_pk_fp8_f32 v158, v72, v76 op_sel:[0,0,1]
	v_cvt_pk_fp8_f32 v159, v88, v92 op_sel:[0,0,1]
	v_cvt_pk_fp8_f32 v160, v104, v108 op_sel:[0,0,1]
	v_cvt_pk_fp8_f32 v161, v120, v124 op_sel:[0,0,1]
	s_nop 0
	global_store_dwordx4 v170, v[158:161], s[20:21]
	v_mul_f32_e32 v65, 0x42000000, v65
	v_mul_f32_e32 v69, 0x42000000, v69
	v_mul_f32_e32 v73, 0x42000000, v73
	v_mul_f32_e32 v77, 0x42000000, v77
	v_mul_f32_e32 v81, 0x42000000, v81
	v_mul_f32_e32 v85, 0x42000000, v85
	v_mul_f32_e32 v89, 0x42000000, v89
	v_mul_f32_e32 v93, 0x42000000, v93
	v_mul_f32_e32 v97, 0x42000000, v97
	v_mul_f32_e32 v101, 0x42000000, v101
	v_mul_f32_e32 v105, 0x42000000, v105
	v_mul_f32_e32 v109, 0x42000000, v109
	v_mul_f32_e32 v113, 0x42000000, v113
	v_mul_f32_e32 v117, 0x42000000, v117
	v_mul_f32_e32 v121, 0x42000000, v121
	v_mul_f32_e32 v125, 0x42000000, v125
	v_med3_f32 v65, v65, s28, v171
	v_med3_f32 v69, v69, s28, v171
	v_med3_f32 v73, v73, s28, v171
	v_med3_f32 v77, v77, s28, v171
	v_med3_f32 v81, v81, s28, v171
	v_med3_f32 v85, v85, s28, v171
	v_med3_f32 v89, v89, s28, v171
	v_med3_f32 v93, v93, s28, v171
	v_med3_f32 v97, v97, s28, v171
	v_med3_f32 v101, v101, s28, v171
	v_med3_f32 v105, v105, s28, v171
	v_med3_f32 v109, v109, s28, v171
	v_med3_f32 v113, v113, s28, v171
	v_med3_f32 v117, v117, s28, v171
	v_med3_f32 v121, v121, s28, v171
	v_med3_f32 v125, v125, s28, v171
	v_cvt_pk_fp8_f32 v162, v65, v69
	v_cvt_pk_fp8_f32 v163, v81, v85
	v_cvt_pk_fp8_f32 v164, v97, v101
	v_cvt_pk_fp8_f32 v165, v113, v117
	v_cvt_pk_fp8_f32 v162, v73, v77 op_sel:[0,0,1]
	v_cvt_pk_fp8_f32 v163, v89, v93 op_sel:[0,0,1]
	v_cvt_pk_fp8_f32 v164, v105, v109 op_sel:[0,0,1]
	v_cvt_pk_fp8_f32 v165, v121, v125 op_sel:[0,0,1]
	s_nop 0
	global_store_dwordx4 v170, v[162:165], s[20:21] offset:1024
	v_mul_f32_e32 v66, 0x42000000, v66
	v_mul_f32_e32 v70, 0x42000000, v70
	v_mul_f32_e32 v74, 0x42000000, v74
	v_mul_f32_e32 v78, 0x42000000, v78
	v_mul_f32_e32 v82, 0x42000000, v82
	v_mul_f32_e32 v86, 0x42000000, v86
	v_mul_f32_e32 v90, 0x42000000, v90
	v_mul_f32_e32 v94, 0x42000000, v94
	v_mul_f32_e32 v98, 0x42000000, v98
	v_mul_f32_e32 v102, 0x42000000, v102
	v_mul_f32_e32 v106, 0x42000000, v106
	v_mul_f32_e32 v110, 0x42000000, v110
	v_mul_f32_e32 v114, 0x42000000, v114
	v_mul_f32_e32 v118, 0x42000000, v118
	v_mul_f32_e32 v122, 0x42000000, v122
	v_mul_f32_e32 v126, 0x42000000, v126
	v_med3_f32 v66, v66, s28, v171
	v_med3_f32 v70, v70, s28, v171
	v_med3_f32 v74, v74, s28, v171
	v_med3_f32 v78, v78, s28, v171
	v_med3_f32 v82, v82, s28, v171
	v_med3_f32 v86, v86, s28, v171
	v_med3_f32 v90, v90, s28, v171
	v_med3_f32 v94, v94, s28, v171
	v_med3_f32 v98, v98, s28, v171
	v_med3_f32 v102, v102, s28, v171
	v_med3_f32 v106, v106, s28, v171
	v_med3_f32 v110, v110, s28, v171
	v_med3_f32 v114, v114, s28, v171
	v_med3_f32 v118, v118, s28, v171
	v_med3_f32 v122, v122, s28, v171
	v_med3_f32 v126, v126, s28, v171
	v_cvt_pk_fp8_f32 v158, v66, v70
	v_cvt_pk_fp8_f32 v159, v82, v86
	v_cvt_pk_fp8_f32 v160, v98, v102
	v_cvt_pk_fp8_f32 v161, v114, v118
	v_cvt_pk_fp8_f32 v158, v74, v78 op_sel:[0,0,1]
	v_cvt_pk_fp8_f32 v159, v90, v94 op_sel:[0,0,1]
	v_cvt_pk_fp8_f32 v160, v106, v110 op_sel:[0,0,1]
	v_cvt_pk_fp8_f32 v161, v122, v126 op_sel:[0,0,1]
	s_nop 0
	global_store_dwordx4 v170, v[158:161], s[20:21] offset:2048
	v_mul_f32_e32 v67, 0x42000000, v67
	v_mul_f32_e32 v71, 0x42000000, v71
	v_mul_f32_e32 v75, 0x42000000, v75
	v_mul_f32_e32 v79, 0x42000000, v79
	v_mul_f32_e32 v83, 0x42000000, v83
	v_mul_f32_e32 v87, 0x42000000, v87
	v_mul_f32_e32 v91, 0x42000000, v91
	v_mul_f32_e32 v95, 0x42000000, v95
	v_mul_f32_e32 v99, 0x42000000, v99
	v_mul_f32_e32 v103, 0x42000000, v103
	v_mul_f32_e32 v107, 0x42000000, v107
	v_mul_f32_e32 v111, 0x42000000, v111
	v_mul_f32_e32 v115, 0x42000000, v115
	v_mul_f32_e32 v119, 0x42000000, v119
	v_mul_f32_e32 v123, 0x42000000, v123
	v_mul_f32_e32 v127, 0x42000000, v127
	v_med3_f32 v67, v67, s28, v171
	v_med3_f32 v71, v71, s28, v171
	v_med3_f32 v75, v75, s28, v171
	v_med3_f32 v79, v79, s28, v171
	v_med3_f32 v83, v83, s28, v171
	v_med3_f32 v87, v87, s28, v171
	v_med3_f32 v91, v91, s28, v171
	v_med3_f32 v95, v95, s28, v171
	v_med3_f32 v99, v99, s28, v171
	v_med3_f32 v103, v103, s28, v171
	v_med3_f32 v107, v107, s28, v171
	v_med3_f32 v111, v111, s28, v171
	v_med3_f32 v115, v115, s28, v171
	v_med3_f32 v119, v119, s28, v171
	v_med3_f32 v123, v123, s28, v171
	v_med3_f32 v127, v127, s28, v171
	v_cvt_pk_fp8_f32 v162, v67, v71
	v_cvt_pk_fp8_f32 v163, v83, v87
	v_cvt_pk_fp8_f32 v164, v99, v103
	v_cvt_pk_fp8_f32 v165, v115, v119
	v_cvt_pk_fp8_f32 v162, v75, v79 op_sel:[0,0,1]
	v_cvt_pk_fp8_f32 v163, v91, v95 op_sel:[0,0,1]
	v_cvt_pk_fp8_f32 v164, v107, v111 op_sel:[0,0,1]
	v_cvt_pk_fp8_f32 v165, v123, v127 op_sel:[0,0,1]
	s_nop 0
	global_store_dwordx4 v170, v[162:165], s[20:21] offset:3072
	s_cmp_ge_u32 s7, s6
	s_cbranch_scc1 .Lp4c1_done
	s_mov_b32 s4, s7
	s_add_i32 s7, s4, s5
	s_cmp_lt_u32 s7, s6
	s_cbranch_scc0 .Lp4c1_A_last
	s_lshr_b32 s22, s7, 8
	s_and_b32 s23, s7, 0xff
	s_and_b32 s27, s22, 1
	s_lshr_b32 s22, s22, 1
	s_cmp_eq_u32 s27, 0
	s_cselect_b64 s[16:17], s[12:13], s[14:15]
	s_add_i32 s22, s22, 37
	s_lshl_b32 s24, s22, 22
	s_lshr_b32 s25, s23, 5
	s_lshl_b32 s25, s25, 19
	s_and_b32 s26, s23, 31
	s_lshl_b32 s26, s26, 7
	s_add_i32 s24, s24, s25
	s_add_i32 s24, s24, s26
	s_add_u32 s16, s16, s24
	s_addc_u32 s17, s17, 0
	s_nop 0
	global_load_dwordx4 v[64:67], v166, s[16:17] nt
	global_load_dwordx4 v[68:71], v167, s[16:17] nt
	global_load_dwordx4 v[72:75], v168, s[16:17] nt
	global_load_dwordx4 v[76:79], v169, s[16:17] nt
	s_add_u32 s16, s16, 0x4000
	s_addc_u32 s17, s17, 0
	s_nop 0
	global_load_dwordx4 v[80:83], v166, s[16:17] nt
	global_load_dwordx4 v[84:87], v167, s[16:17] nt
	global_load_dwordx4 v[88:91], v168, s[16:17] nt
	global_load_dwordx4 v[92:95], v169, s[16:17] nt
	s_add_u32 s16, s16, 0x4000
	s_addc_u32 s17, s17, 0
	s_nop 0
	global_load_dwordx4 v[96:99], v166, s[16:17] nt
	global_load_dwordx4 v[100:103], v167, s[16:17] nt
	global_load_dwordx4 v[104:107], v168, s[16:17] nt
	global_load_dwordx4 v[108:111], v169, s[16:17] nt
	s_add_u32 s16, s16, 0x4000
	s_addc_u32 s17, s17, 0
	s_nop 0
	global_load_dwordx4 v[112:115], v166, s[16:17] nt
	global_load_dwordx4 v[116:119], v167, s[16:17] nt
	global_load_dwordx4 v[120:123], v168, s[16:17] nt
	global_load_dwordx4 v[124:127], v169, s[16:17] nt
	s_waitcnt vmcnt(20)
	s_branch .Lp4c1_A_st

.Lp4c1_A_st:
	s_lshr_b32 s22, s4, 8
	s_and_b32 s23, s4, 0xff
	s_and_b32 s27, s22, 1
	s_lshr_b32 s22, s22, 1
	s_add_i32 s22, s22, 37
	s_mul_i32 s24, s22, 0x300000
	s_lshr_b32 s25, s23, 5
	s_lshl_b32 s25, s25, 7
	s_add_i32 s24, s24, s25
	s_and_b32 s26, s23, 31
	s_lshr_b32 s25, s26, 2
	s_lshl_b32 s25, s25, 18
	s_add_i32 s24, s24, s25
	s_lshl_b32 s25, s27, 17
	s_add_i32 s24, s24, s25
	s_and_b32 s25, s26, 3
	s_lshl_b32 s25, s25, 15
	s_add_i32 s24, s24, s25
	s_add_u32 s20, s10, s24
	s_addc_u32 s21, s11, 0
	v_mul_f32_e32 v0, 0x42000000, v0
	v_mul_f32_e32 v4, 0x42000000, v4
	v_mul_f32_e32 v8, 0x42000000, v8
	v_mul_f32_e32 v12, 0x42000000, v12
	v_mul_f32_e32 v16, 0x42000000, v16
	v_mul_f32_e32 v20, 0x42000000, v20
	v_mul_f32_e32 v24, 0x42000000, v24
	v_mul_f32_e32 v28, 0x42000000, v28
	v_mul_f32_e32 v32, 0x42000000, v32
	v_mul_f32_e32 v36, 0x42000000, v36
	v_mul_f32_e32 v40, 0x42000000, v40
	v_mul_f32_e32 v44, 0x42000000, v44
	v_mul_f32_e32 v48, 0x42000000, v48
	v_mul_f32_e32 v52, 0x42000000, v52
	v_mul_f32_e32 v56, 0x42000000, v56
	v_mul_f32_e32 v60, 0x42000000, v60
	v_med3_f32 v0, v0, s28, v171
	v_med3_f32 v4, v4, s28, v171
	v_med3_f32 v8, v8, s28, v171
	v_med3_f32 v12, v12, s28, v171
	v_med3_f32 v16, v16, s28, v171
	v_med3_f32 v20, v20, s28, v171
	v_med3_f32 v24, v24, s28, v171
	v_med3_f32 v28, v28, s28, v171
	v_med3_f32 v32, v32, s28, v171
	v_med3_f32 v36, v36, s28, v171
	v_med3_f32 v40, v40, s28, v171
	v_med3_f32 v44, v44, s28, v171
	v_med3_f32 v48, v48, s28, v171
	v_med3_f32 v52, v52, s28, v171
	v_med3_f32 v56, v56, s28, v171
	v_med3_f32 v60, v60, s28, v171
	v_cvt_pk_fp8_f32 v158, v0, v4
	v_cvt_pk_fp8_f32 v159, v16, v20
	v_cvt_pk_fp8_f32 v160, v32, v36
	v_cvt_pk_fp8_f32 v161, v48, v52
	v_cvt_pk_fp8_f32 v158, v8, v12 op_sel:[0,0,1]
	v_cvt_pk_fp8_f32 v159, v24, v28 op_sel:[0,0,1]
	v_cvt_pk_fp8_f32 v160, v40, v44 op_sel:[0,0,1]
	v_cvt_pk_fp8_f32 v161, v56, v60 op_sel:[0,0,1]
	s_nop 0
	global_store_dwordx4 v170, v[158:161], s[20:21]
	v_mul_f32_e32 v1, 0x42000000, v1
	v_mul_f32_e32 v5, 0x42000000, v5
	v_mul_f32_e32 v9, 0x42000000, v9
	v_mul_f32_e32 v13, 0x42000000, v13
	v_mul_f32_e32 v17, 0x42000000, v17
	v_mul_f32_e32 v21, 0x42000000, v21
	v_mul_f32_e32 v25, 0x42000000, v25
	v_mul_f32_e32 v29, 0x42000000, v29
	v_mul_f32_e32 v33, 0x42000000, v33
	v_mul_f32_e32 v37, 0x42000000, v37
	v_mul_f32_e32 v41, 0x42000000, v41
	v_mul_f32_e32 v45, 0x42000000, v45
	v_mul_f32_e32 v49, 0x42000000, v49
	v_mul_f32_e32 v53, 0x42000000, v53
	v_mul_f32_e32 v57, 0x42000000, v57
	v_mul_f32_e32 v61, 0x42000000, v61
	v_med3_f32 v1, v1, s28, v171
	v_med3_f32 v5, v5, s28, v171
	v_med3_f32 v9, v9, s28, v171
	v_med3_f32 v13, v13, s28, v171
	v_med3_f32 v17, v17, s28, v171
	v_med3_f32 v21, v21, s28, v171
	v_med3_f32 v25, v25, s28, v171
	v_med3_f32 v29, v29, s28, v171
	v_med3_f32 v33, v33, s28, v171
	v_med3_f32 v37, v37, s28, v171
	v_med3_f32 v41, v41, s28, v171
	v_med3_f32 v45, v45, s28, v171
	v_med3_f32 v49, v49, s28, v171
	v_med3_f32 v53, v53, s28, v171
	v_med3_f32 v57, v57, s28, v171
	v_med3_f32 v61, v61, s28, v171
	v_cvt_pk_fp8_f32 v162, v1, v5
	v_cvt_pk_fp8_f32 v163, v17, v21
	v_cvt_pk_fp8_f32 v164, v33, v37
	v_cvt_pk_fp8_f32 v165, v49, v53
	v_cvt_pk_fp8_f32 v162, v9, v13 op_sel:[0,0,1]
	v_cvt_pk_fp8_f32 v163, v25, v29 op_sel:[0,0,1]
	v_cvt_pk_fp8_f32 v164, v41, v45 op_sel:[0,0,1]
	v_cvt_pk_fp8_f32 v165, v57, v61 op_sel:[0,0,1]
	s_nop 0
	global_store_dwordx4 v170, v[162:165], s[20:21] offset:1024
	v_mul_f32_e32 v2, 0x42000000, v2
	v_mul_f32_e32 v6, 0x42000000, v6
	v_mul_f32_e32 v10, 0x42000000, v10
	v_mul_f32_e32 v14, 0x42000000, v14
	v_mul_f32_e32 v18, 0x42000000, v18
	v_mul_f32_e32 v22, 0x42000000, v22
	v_mul_f32_e32 v26, 0x42000000, v26
	v_mul_f32_e32 v30, 0x42000000, v30
	v_mul_f32_e32 v34, 0x42000000, v34
	v_mul_f32_e32 v38, 0x42000000, v38
	v_mul_f32_e32 v42, 0x42000000, v42
	v_mul_f32_e32 v46, 0x42000000, v46
	v_mul_f32_e32 v50, 0x42000000, v50
	v_mul_f32_e32 v54, 0x42000000, v54
	v_mul_f32_e32 v58, 0x42000000, v58
	v_mul_f32_e32 v62, 0x42000000, v62
	v_med3_f32 v2, v2, s28, v171
	v_med3_f32 v6, v6, s28, v171
	v_med3_f32 v10, v10, s28, v171
	v_med3_f32 v14, v14, s28, v171
	v_med3_f32 v18, v18, s28, v171
	v_med3_f32 v22, v22, s28, v171
	v_med3_f32 v26, v26, s28, v171
	v_med3_f32 v30, v30, s28, v171
	v_med3_f32 v34, v34, s28, v171
	v_med3_f32 v38, v38, s28, v171
	v_med3_f32 v42, v42, s28, v171
	v_med3_f32 v46, v46, s28, v171
	v_med3_f32 v50, v50, s28, v171
	v_med3_f32 v54, v54, s28, v171
	v_med3_f32 v58, v58, s28, v171
	v_med3_f32 v62, v62, s28, v171
	v_cvt_pk_fp8_f32 v158, v2, v6
	v_cvt_pk_fp8_f32 v159, v18, v22
	v_cvt_pk_fp8_f32 v160, v34, v38
	v_cvt_pk_fp8_f32 v161, v50, v54
	v_cvt_pk_fp8_f32 v158, v10, v14 op_sel:[0,0,1]
	v_cvt_pk_fp8_f32 v159, v26, v30 op_sel:[0,0,1]
	v_cvt_pk_fp8_f32 v160, v42, v46 op_sel:[0,0,1]
	v_cvt_pk_fp8_f32 v161, v58, v62 op_sel:[0,0,1]
	s_nop 0
	global_store_dwordx4 v170, v[158:161], s[20:21] offset:2048
	v_mul_f32_e32 v3, 0x42000000, v3
	v_mul_f32_e32 v7, 0x42000000, v7
	v_mul_f32_e32 v11, 0x42000000, v11
	v_mul_f32_e32 v15, 0x42000000, v15
	v_mul_f32_e32 v19, 0x42000000, v19
	v_mul_f32_e32 v23, 0x42000000, v23
	v_mul_f32_e32 v27, 0x42000000, v27
	v_mul_f32_e32 v31, 0x42000000, v31
	v_mul_f32_e32 v35, 0x42000000, v35
	v_mul_f32_e32 v39, 0x42000000, v39
	v_mul_f32_e32 v43, 0x42000000, v43
	v_mul_f32_e32 v47, 0x42000000, v47
	v_mul_f32_e32 v51, 0x42000000, v51
	v_mul_f32_e32 v55, 0x42000000, v55
	v_mul_f32_e32 v59, 0x42000000, v59
	v_mul_f32_e32 v63, 0x42000000, v63
	v_med3_f32 v3, v3, s28, v171
	v_med3_f32 v7, v7, s28, v171
	v_med3_f32 v11, v11, s28, v171
	v_med3_f32 v15, v15, s28, v171
	v_med3_f32 v19, v19, s28, v171
	v_med3_f32 v23, v23, s28, v171
	v_med3_f32 v27, v27, s28, v171
	v_med3_f32 v31, v31, s28, v171
	v_med3_f32 v35, v35, s28, v171
	v_med3_f32 v39, v39, s28, v171
	v_med3_f32 v43, v43, s28, v171
	v_med3_f32 v47, v47, s28, v171
	v_med3_f32 v51, v51, s28, v171
	v_med3_f32 v55, v55, s28, v171
	v_med3_f32 v59, v59, s28, v171
	v_med3_f32 v63, v63, s28, v171
	v_cvt_pk_fp8_f32 v162, v3, v7
	v_cvt_pk_fp8_f32 v163, v19, v23
	v_cvt_pk_fp8_f32 v164, v35, v39
	v_cvt_pk_fp8_f32 v165, v51, v55
	v_cvt_pk_fp8_f32 v162, v11, v15 op_sel:[0,0,1]
	v_cvt_pk_fp8_f32 v163, v27, v31 op_sel:[0,0,1]
	v_cvt_pk_fp8_f32 v164, v43, v47 op_sel:[0,0,1]
	v_cvt_pk_fp8_f32 v165, v59, v63 op_sel:[0,0,1]
	s_nop 0
	global_store_dwordx4 v170, v[162:165], s[20:21] offset:3072
	s_cmp_ge_u32 s7, s6
	s_cbranch_scc1 .Lp4c1_done
	s_mov_b32 s4, s7
	s_branch .Lp4c1_loop

.LBB0_1234:
	s_load_dwordx4 s[0:3], s[8:9], 0x138
	s_waitcnt lgkmcnt(0)
	s_mov_b64 s[4:5], s[0:1]
	s_cmp_lt_i32 s4, 10
	s_cselect_b64 s[0:1], -1, 0
	s_cmp_gt_i32 s5, 9
	s_cselect_b64 s[2:3], -1, 0
	s_and_b64 s[0:1], s[0:1], s[2:3]
	s_andn2_b64 vcc, exec, s[0:1]
	s_cbranch_vccnz .LBB0_1372
	s_mov_b64 s[0:1], s[8:9]
	v_mbcnt_lo_u32_b32 v146, -1, 0
	v_mbcnt_hi_u32_b32 v146, -1, v146
	s_load_dword s38, s[8:9], 0x148
	s_add_u32 s4, s8, 0x148
	v_readlane_b32 s2, v243, 0
	s_addc_u32 s5, s9, 0
	v_readlane_b32 s3, v243, 1
	s_waitcnt lgkmcnt(0)
	s_sub_i32 s39, s38, 44
	s_cmp_lt_i32 s2, s39
	s_mov_b64 s[2:3], -1
	s_cbranch_scc1 .LBB0_1257
	s_mov_b64 s[30:31], s[4:5]
	v_readlane_b32 s4, v243, 0
	s_sub_i32 s4, s4, s39
	s_lshl_b32 s4, s4, 3
	s_add_i32 s19, s4, s94
	s_mov_b32 s4, s19
	s_mov_b32 s5, 0x160
	s_mov_b32 s6, 0xe00
	s_waitcnt vmcnt(0)
	s_cmp_ge_u32 s4, s6
	s_cbranch_scc1 .Lp9c0_done
	v_readlane_b32 s8, v243, 7
	v_readlane_b32 s9, v243, 8
	s_load_dwordx2 s[10:11], s[8:9], 0x130
	s_load_dwordx2 s[12:13], s[8:9], 0xf8
	s_load_dwordx2 s[14:15], s[8:9], 0x108
	v_mbcnt_lo_u32_b32 v162, -1, 0
	v_mbcnt_hi_u32_b32 v162, -1, v162
	v_lshrrev_b32_e32 v163, 3, v162
	v_and_b32_e32 v162, 7, v162
	v_lshlrev_b32_e32 v156, 16, v163
	v_lshl_add_u32 v156, v162, 4, v156
	v_add_u32_e32 v157, 0x1000, v156
	v_add_u32_e32 v158, 0x2000, v156
	v_add_u32_e32 v159, 0x3000, v156
	v_lshlrev_b32_e32 v160, 12, v162
	v_lshl_add_u32 v160, v163, 4, v160
	v_mov_b32_e32 v161, 0x43e00000
	s_mov_b32 s28, 0xc3e00000
	s_waitcnt lgkmcnt(0)
	s_add_u32 s10, s10, 0x2900000
	s_addc_u32 s11, s11, 0
	s_lshr_b32 s22, s4, 8
	s_and_b32 s23, s4, 0xff
	s_and_b32 s27, s22, 1
	s_lshr_b32 s22, s22, 1
	s_cmp_eq_u32 s27, 0
	s_cselect_b64 s[16:17], s[12:13], s[14:15]
	s_add_i32 s22, s22, 40
	s_lshl_b32 s24, s22, 22
	s_lshr_b32 s25, s23, 5
	s_lshl_b32 s25, s25, 19
	s_and_b32 s26, s23, 31
	s_lshl_b32 s26, s26, 7
	s_add_i32 s24, s24, s25
	s_add_i32 s24, s24, s26
	s_add_u32 s16, s16, s24
	s_addc_u32 s17, s17, 0
	s_nop 0
	global_load_dwordx4 v[0:3], v156, s[16:17] nt
	global_load_dwordx4 v[4:7], v157, s[16:17] nt
	global_load_dwordx4 v[8:11], v158, s[16:17] nt
	global_load_dwordx4 v[12:15], v159, s[16:17] nt
	s_add_u32 s16, s16, 0x4000
	s_addc_u32 s17, s17, 0
	s_nop 0
	global_load_dwordx4 v[16:19], v156, s[16:17] nt
	global_load_dwordx4 v[20:23], v157, s[16:17] nt
	global_load_dwordx4 v[24:27], v158, s[16:17] nt
	global_load_dwordx4 v[28:31], v159, s[16:17] nt
	s_add_u32 s16, s16, 0x4000
	s_addc_u32 s17, s17, 0
	s_nop 0
	global_load_dwordx4 v[32:35], v156, s[16:17] nt
	global_load_dwordx4 v[36:39], v157, s[16:17] nt
	global_load_dwordx4 v[40:43], v158, s[16:17] nt
	global_load_dwordx4 v[44:47], v159, s[16:17] nt
	s_add_u32 s16, s16, 0x4000
	s_addc_u32 s17, s17, 0
	s_nop 0
	global_load_dwordx4 v[48:51], v156, s[16:17] nt
	global_load_dwordx4 v[52:55], v157, s[16:17] nt
	global_load_dwordx4 v[56:59], v158, s[16:17] nt
	global_load_dwordx4 v[60:63], v159, s[16:17] nt
	s_add_i32 s7, s4, s5
	s_cmp_lt_u32 s7, s6
	s_cbranch_scc0 .Lp9c0_p_last
	s_lshr_b32 s22, s7, 8
	s_and_b32 s23, s7, 0xff
	s_and_b32 s27, s22, 1
	s_lshr_b32 s22, s22, 1
	s_cmp_eq_u32 s27, 0
	s_cselect_b64 s[16:17], s[12:13], s[14:15]
	s_add_i32 s22, s22, 40
	s_lshl_b32 s24, s22, 22
	s_lshr_b32 s25, s23, 5
	s_lshl_b32 s25, s25, 19
	s_and_b32 s26, s23, 31
	s_lshl_b32 s26, s26, 7
	s_add_i32 s24, s24, s25
	s_add_i32 s24, s24, s26
	s_add_u32 s16, s16, s24
	s_addc_u32 s17, s17, 0
	s_nop 0
	global_load_dwordx4 v[64:67], v156, s[16:17] nt
	global_load_dwordx4 v[68:71], v157, s[16:17] nt
	global_load_dwordx4 v[72:75], v158, s[16:17] nt
	global_load_dwordx4 v[76:79], v159, s[16:17] nt
	s_add_u32 s16, s16, 0x4000
	s_addc_u32 s17, s17, 0
	s_nop 0
	global_load_dwordx4 v[80:83], v156, s[16:17] nt
	global_load_dwordx4 v[84:87], v157, s[16:17] nt
	global_load_dwordx4 v[88:91], v158, s[16:17] nt
	global_load_dwordx4 v[92:95], v159, s[16:17] nt
	s_add_u32 s16, s16, 0x4000
	s_addc_u32 s17, s17, 0
	s_nop 0
	global_load_dwordx4 v[96:99], v156, s[16:17] nt
	global_load_dwordx4 v[100:103], v157, s[16:17] nt
	global_load_dwordx4 v[104:107], v158, s[16:17] nt
	global_load_dwordx4 v[108:111], v159, s[16:17] nt
	s_add_u32 s16, s16, 0x4000
	s_addc_u32 s17, s17, 0
	s_nop 0
	global_load_dwordx4 v[112:115], v156, s[16:17] nt
	global_load_dwordx4 v[116:119], v157, s[16:17] nt
	global_load_dwordx4 v[120:123], v158, s[16:17] nt
	global_load_dwordx4 v[124:127], v159, s[16:17] nt
	s_waitcnt vmcnt(16)
	s_branch .Lp9c0_p_st

.Lp9c0_p_st:
	s_lshr_b32 s22, s4, 8
	s_and_b32 s23, s4, 0xff
	s_and_b32 s27, s22, 1
	s_lshr_b32 s22, s22, 1
	s_add_i32 s22, s22, 40
	s_mul_i32 s24, s22, 0x300000
	s_lshr_b32 s25, s23, 5
	s_lshl_b32 s25, s25, 7
	s_add_i32 s24, s24, s25
	s_and_b32 s26, s23, 31
	s_lshr_b32 s25, s26, 2
	s_lshl_b32 s25, s25, 18
	s_add_i32 s24, s24, s25
	s_lshl_b32 s25, s27, 17
	s_add_i32 s24, s24, s25
	s_and_b32 s25, s26, 3
	s_lshl_b32 s25, s25, 15
	s_add_i32 s24, s24, s25
	s_add_u32 s20, s10, s24
	s_addc_u32 s21, s11, 0
	v_mul_f32_e32 v0, 0x42000000, v0
	v_mul_f32_e32 v4, 0x42000000, v4
	v_mul_f32_e32 v8, 0x42000000, v8
	v_mul_f32_e32 v12, 0x42000000, v12
	v_mul_f32_e32 v16, 0x42000000, v16
	v_mul_f32_e32 v20, 0x42000000, v20
	v_mul_f32_e32 v24, 0x42000000, v24
	v_mul_f32_e32 v28, 0x42000000, v28
	v_mul_f32_e32 v32, 0x42000000, v32
	v_mul_f32_e32 v36, 0x42000000, v36
	v_mul_f32_e32 v40, 0x42000000, v40
	v_mul_f32_e32 v44, 0x42000000, v44
	v_mul_f32_e32 v48, 0x42000000, v48
	v_mul_f32_e32 v52, 0x42000000, v52
	v_mul_f32_e32 v56, 0x42000000, v56
	v_mul_f32_e32 v60, 0x42000000, v60
	v_med3_f32 v0, v0, s28, v161
	v_med3_f32 v4, v4, s28, v161
	v_med3_f32 v8, v8, s28, v161
	v_med3_f32 v12, v12, s28, v161
	v_med3_f32 v16, v16, s28, v161
	v_med3_f32 v20, v20, s28, v161
	v_med3_f32 v24, v24, s28, v161
	v_med3_f32 v28, v28, s28, v161
	v_med3_f32 v32, v32, s28, v161
	v_med3_f32 v36, v36, s28, v161
	v_med3_f32 v40, v40, s28, v161
	v_med3_f32 v44, v44, s28, v161
	v_med3_f32 v48, v48, s28, v161
	v_med3_f32 v52, v52, s28, v161
	v_med3_f32 v56, v56, s28, v161
	v_med3_f32 v60, v60, s28, v161
	v_cvt_pk_fp8_f32 v148, v0, v4
	v_cvt_pk_fp8_f32 v149, v16, v20
	v_cvt_pk_fp8_f32 v150, v32, v36
	v_cvt_pk_fp8_f32 v151, v48, v52
	v_cvt_pk_fp8_f32 v148, v8, v12 op_sel:[0,0,1]
	v_cvt_pk_fp8_f32 v149, v24, v28 op_sel:[0,0,1]
	v_cvt_pk_fp8_f32 v150, v40, v44 op_sel:[0,0,1]
	v_cvt_pk_fp8_f32 v151, v56, v60 op_sel:[0,0,1]
	s_nop 0
	global_store_dwordx4 v160, v[148:151], s[20:21]
	v_mul_f32_e32 v1, 0x42000000, v1
	v_mul_f32_e32 v5, 0x42000000, v5
	v_mul_f32_e32 v9, 0x42000000, v9
	v_mul_f32_e32 v13, 0x42000000, v13
	v_mul_f32_e32 v17, 0x42000000, v17
	v_mul_f32_e32 v21, 0x42000000, v21
	v_mul_f32_e32 v25, 0x42000000, v25
	v_mul_f32_e32 v29, 0x42000000, v29
	v_mul_f32_e32 v33, 0x42000000, v33
	v_mul_f32_e32 v37, 0x42000000, v37
	v_mul_f32_e32 v41, 0x42000000, v41
	v_mul_f32_e32 v45, 0x42000000, v45
	v_mul_f32_e32 v49, 0x42000000, v49
	v_mul_f32_e32 v53, 0x42000000, v53
	v_mul_f32_e32 v57, 0x42000000, v57
	v_mul_f32_e32 v61, 0x42000000, v61
	v_med3_f32 v1, v1, s28, v161
	v_med3_f32 v5, v5, s28, v161
	v_med3_f32 v9, v9, s28, v161
	v_med3_f32 v13, v13, s28, v161
	v_med3_f32 v17, v17, s28, v161
	v_med3_f32 v21, v21, s28, v161
	v_med3_f32 v25, v25, s28, v161
	v_med3_f32 v29, v29, s28, v161
	v_med3_f32 v33, v33, s28, v161
	v_med3_f32 v37, v37, s28, v161
	v_med3_f32 v41, v41, s28, v161
	v_med3_f32 v45, v45, s28, v161
	v_med3_f32 v49, v49, s28, v161
	v_med3_f32 v53, v53, s28, v161
	v_med3_f32 v57, v57, s28, v161
	v_med3_f32 v61, v61, s28, v161
	v_cvt_pk_fp8_f32 v152, v1, v5
	v_cvt_pk_fp8_f32 v153, v17, v21
	v_cvt_pk_fp8_f32 v154, v33, v37
	v_cvt_pk_fp8_f32 v155, v49, v53
	v_cvt_pk_fp8_f32 v152, v9, v13 op_sel:[0,0,1]
	v_cvt_pk_fp8_f32 v153, v25, v29 op_sel:[0,0,1]
	v_cvt_pk_fp8_f32 v154, v41, v45 op_sel:[0,0,1]
	v_cvt_pk_fp8_f32 v155, v57, v61 op_sel:[0,0,1]
	s_nop 0
	global_store_dwordx4 v160, v[152:155], s[20:21] offset:1024
	v_mul_f32_e32 v2, 0x42000000, v2
	v_mul_f32_e32 v6, 0x42000000, v6
	v_mul_f32_e32 v10, 0x42000000, v10
	v_mul_f32_e32 v14, 0x42000000, v14
	v_mul_f32_e32 v18, 0x42000000, v18
	v_mul_f32_e32 v22, 0x42000000, v22
	v_mul_f32_e32 v26, 0x42000000, v26
	v_mul_f32_e32 v30, 0x42000000, v30
	v_mul_f32_e32 v34, 0x42000000, v34
	v_mul_f32_e32 v38, 0x42000000, v38
	v_mul_f32_e32 v42, 0x42000000, v42
	v_mul_f32_e32 v46, 0x42000000, v46
	v_mul_f32_e32 v50, 0x42000000, v50
	v_mul_f32_e32 v54, 0x42000000, v54
	v_mul_f32_e32 v58, 0x42000000, v58
	v_mul_f32_e32 v62, 0x42000000, v62
	v_med3_f32 v2, v2, s28, v161
	v_med3_f32 v6, v6, s28, v161
	v_med3_f32 v10, v10, s28, v161
	v_med3_f32 v14, v14, s28, v161
	v_med3_f32 v18, v18, s28, v161
	v_med3_f32 v22, v22, s28, v161
	v_med3_f32 v26, v26, s28, v161
	v_med3_f32 v30, v30, s28, v161
	v_med3_f32 v34, v34, s28, v161
	v_med3_f32 v38, v38, s28, v161
	v_med3_f32 v42, v42, s28, v161
	v_med3_f32 v46, v46, s28, v161
	v_med3_f32 v50, v50, s28, v161
	v_med3_f32 v54, v54, s28, v161
	v_med3_f32 v58, v58, s28, v161
	v_med3_f32 v62, v62, s28, v161
	v_cvt_pk_fp8_f32 v148, v2, v6
	v_cvt_pk_fp8_f32 v149, v18, v22
	v_cvt_pk_fp8_f32 v150, v34, v38
	v_cvt_pk_fp8_f32 v151, v50, v54
	v_cvt_pk_fp8_f32 v148, v10, v14 op_sel:[0,0,1]
	v_cvt_pk_fp8_f32 v149, v26, v30 op_sel:[0,0,1]
	v_cvt_pk_fp8_f32 v150, v42, v46 op_sel:[0,0,1]
	v_cvt_pk_fp8_f32 v151, v58, v62 op_sel:[0,0,1]
	s_nop 0
	global_store_dwordx4 v160, v[148:151], s[20:21] offset:2048
	v_mul_f32_e32 v3, 0x42000000, v3
	v_mul_f32_e32 v7, 0x42000000, v7
	v_mul_f32_e32 v11, 0x42000000, v11
	v_mul_f32_e32 v15, 0x42000000, v15
	v_mul_f32_e32 v19, 0x42000000, v19
	v_mul_f32_e32 v23, 0x42000000, v23
	v_mul_f32_e32 v27, 0x42000000, v27
	v_mul_f32_e32 v31, 0x42000000, v31
	v_mul_f32_e32 v35, 0x42000000, v35
	v_mul_f32_e32 v39, 0x42000000, v39
	v_mul_f32_e32 v43, 0x42000000, v43
	v_mul_f32_e32 v47, 0x42000000, v47
	v_mul_f32_e32 v51, 0x42000000, v51
	v_mul_f32_e32 v55, 0x42000000, v55
	v_mul_f32_e32 v59, 0x42000000, v59
	v_mul_f32_e32 v63, 0x42000000, v63
	v_med3_f32 v3, v3, s28, v161
	v_med3_f32 v7, v7, s28, v161
	v_med3_f32 v11, v11, s28, v161
	v_med3_f32 v15, v15, s28, v161
	v_med3_f32 v19, v19, s28, v161
	v_med3_f32 v23, v23, s28, v161
	v_med3_f32 v27, v27, s28, v161
	v_med3_f32 v31, v31, s28, v161
	v_med3_f32 v35, v35, s28, v161
	v_med3_f32 v39, v39, s28, v161
	v_med3_f32 v43, v43, s28, v161
	v_med3_f32 v47, v47, s28, v161
	v_med3_f32 v51, v51, s28, v161
	v_med3_f32 v55, v55, s28, v161
	v_med3_f32 v59, v59, s28, v161
	v_med3_f32 v63, v63, s28, v161
	v_cvt_pk_fp8_f32 v152, v3, v7
	v_cvt_pk_fp8_f32 v153, v19, v23
	v_cvt_pk_fp8_f32 v154, v35, v39
	v_cvt_pk_fp8_f32 v155, v51, v55
	v_cvt_pk_fp8_f32 v152, v11, v15 op_sel:[0,0,1]
	v_cvt_pk_fp8_f32 v153, v27, v31 op_sel:[0,0,1]
	v_cvt_pk_fp8_f32 v154, v43, v47 op_sel:[0,0,1]
	v_cvt_pk_fp8_f32 v155, v59, v63 op_sel:[0,0,1]
	s_nop 0
	global_store_dwordx4 v160, v[152:155], s[20:21] offset:3072
	s_cmp_ge_u32 s7, s6
	s_cbranch_scc1 .Lp9c0_done
	s_mov_b32 s4, s7
.Lp9c0_loop:
	s_add_i32 s7, s4, s5
	s_cmp_lt_u32 s7, s6
	s_cbranch_scc0 .Lp9c0_B_last
	s_lshr_b32 s22, s7, 8
	s_and_b32 s23, s7, 0xff
	s_and_b32 s27, s22, 1
	s_lshr_b32 s22, s22, 1
	s_cmp_eq_u32 s27, 0
	s_cselect_b64 s[16:17], s[12:13], s[14:15]
	s_add_i32 s22, s22, 40
	s_lshl_b32 s24, s22, 22
	s_lshr_b32 s25, s23, 5
	s_lshl_b32 s25, s25, 19
	s_and_b32 s26, s23, 31
	s_lshl_b32 s26, s26, 7
	s_add_i32 s24, s24, s25
	s_add_i32 s24, s24, s26
	s_add_u32 s16, s16, s24
	s_addc_u32 s17, s17, 0
	s_nop 0
	global_load_dwordx4 v[0:3], v156, s[16:17] nt
	global_load_dwordx4 v[4:7], v157, s[16:17] nt
	global_load_dwordx4 v[8:11], v158, s[16:17] nt
	global_load_dwordx4 v[12:15], v159, s[16:17] nt
	s_add_u32 s16, s16, 0x4000
	s_addc_u32 s17, s17, 0
	s_nop 0
	global_load_dwordx4 v[16:19], v156, s[16:17] nt
	global_load_dwordx4 v[20:23], v157, s[16:17] nt
	global_load_dwordx4 v[24:27], v158, s[16:17] nt
	global_load_dwordx4 v[28:31], v159, s[16:17] nt
	s_add_u32 s16, s16, 0x4000
	s_addc_u32 s17, s17, 0
	s_nop 0
	global_load_dwordx4 v[32:35], v156, s[16:17] nt
	global_load_dwordx4 v[36:39], v157, s[16:17] nt
	global_load_dwordx4 v[40:43], v158, s[16:17] nt
	global_load_dwordx4 v[44:47], v159, s[16:17] nt
	s_add_u32 s16, s16, 0x4000
	s_addc_u32 s17, s17, 0
	s_nop 0
	global_load_dwordx4 v[48:51], v156, s[16:17] nt
	global_load_dwordx4 v[52:55], v157, s[16:17] nt
	global_load_dwordx4 v[56:59], v158, s[16:17] nt
	global_load_dwordx4 v[60:63], v159, s[16:17] nt
	s_waitcnt vmcnt(20)
	s_branch .Lp9c0_B_st

.Lp9c0_B_st:
	s_lshr_b32 s22, s4, 8
	s_and_b32 s23, s4, 0xff
	s_and_b32 s27, s22, 1
	s_lshr_b32 s22, s22, 1
	s_add_i32 s22, s22, 40
	s_mul_i32 s24, s22, 0x300000
	s_lshr_b32 s25, s23, 5
	s_lshl_b32 s25, s25, 7
	s_add_i32 s24, s24, s25
	s_and_b32 s26, s23, 31
	s_lshr_b32 s25, s26, 2
	s_lshl_b32 s25, s25, 18
	s_add_i32 s24, s24, s25
	s_lshl_b32 s25, s27, 17
	s_add_i32 s24, s24, s25
	s_and_b32 s25, s26, 3
	s_lshl_b32 s25, s25, 15
	s_add_i32 s24, s24, s25
	s_add_u32 s20, s10, s24
	s_addc_u32 s21, s11, 0
	v_mul_f32_e32 v64, 0x42000000, v64
	v_mul_f32_e32 v68, 0x42000000, v68
	v_mul_f32_e32 v72, 0x42000000, v72
	v_mul_f32_e32 v76, 0x42000000, v76
	v_mul_f32_e32 v80, 0x42000000, v80
	v_mul_f32_e32 v84, 0x42000000, v84
	v_mul_f32_e32 v88, 0x42000000, v88
	v_mul_f32_e32 v92, 0x42000000, v92
	v_mul_f32_e32 v96, 0x42000000, v96
	v_mul_f32_e32 v100, 0x42000000, v100
	v_mul_f32_e32 v104, 0x42000000, v104
	v_mul_f32_e32 v108, 0x42000000, v108
	v_mul_f32_e32 v112, 0x42000000, v112
	v_mul_f32_e32 v116, 0x42000000, v116
	v_mul_f32_e32 v120, 0x42000000, v120
	v_mul_f32_e32 v124, 0x42000000, v124
	v_med3_f32 v64, v64, s28, v161
	v_med3_f32 v68, v68, s28, v161
	v_med3_f32 v72, v72, s28, v161
	v_med3_f32 v76, v76, s28, v161
	v_med3_f32 v80, v80, s28, v161
	v_med3_f32 v84, v84, s28, v161
	v_med3_f32 v88, v88, s28, v161
	v_med3_f32 v92, v92, s28, v161
	v_med3_f32 v96, v96, s28, v161
	v_med3_f32 v100, v100, s28, v161
	v_med3_f32 v104, v104, s28, v161
	v_med3_f32 v108, v108, s28, v161
	v_med3_f32 v112, v112, s28, v161
	v_med3_f32 v116, v116, s28, v161
	v_med3_f32 v120, v120, s28, v161
	v_med3_f32 v124, v124, s28, v161
	v_cvt_pk_fp8_f32 v148, v64, v68
	v_cvt_pk_fp8_f32 v149, v80, v84
	v_cvt_pk_fp8_f32 v150, v96, v100
	v_cvt_pk_fp8_f32 v151, v112, v116
	v_cvt_pk_fp8_f32 v148, v72, v76 op_sel:[0,0,1]
	v_cvt_pk_fp8_f32 v149, v88, v92 op_sel:[0,0,1]
	v_cvt_pk_fp8_f32 v150, v104, v108 op_sel:[0,0,1]
	v_cvt_pk_fp8_f32 v151, v120, v124 op_sel:[0,0,1]
	s_nop 0
	global_store_dwordx4 v160, v[148:151], s[20:21]
	v_mul_f32_e32 v65, 0x42000000, v65
	v_mul_f32_e32 v69, 0x42000000, v69
	v_mul_f32_e32 v73, 0x42000000, v73
	v_mul_f32_e32 v77, 0x42000000, v77
	v_mul_f32_e32 v81, 0x42000000, v81
	v_mul_f32_e32 v85, 0x42000000, v85
	v_mul_f32_e32 v89, 0x42000000, v89
	v_mul_f32_e32 v93, 0x42000000, v93
	v_mul_f32_e32 v97, 0x42000000, v97
	v_mul_f32_e32 v101, 0x42000000, v101
	v_mul_f32_e32 v105, 0x42000000, v105
	v_mul_f32_e32 v109, 0x42000000, v109
	v_mul_f32_e32 v113, 0x42000000, v113
	v_mul_f32_e32 v117, 0x42000000, v117
	v_mul_f32_e32 v121, 0x42000000, v121
	v_mul_f32_e32 v125, 0x42000000, v125
	v_med3_f32 v65, v65, s28, v161
	v_med3_f32 v69, v69, s28, v161
	v_med3_f32 v73, v73, s28, v161
	v_med3_f32 v77, v77, s28, v161
	v_med3_f32 v81, v81, s28, v161
	v_med3_f32 v85, v85, s28, v161
	v_med3_f32 v89, v89, s28, v161
	v_med3_f32 v93, v93, s28, v161
	v_med3_f32 v97, v97, s28, v161
	v_med3_f32 v101, v101, s28, v161
	v_med3_f32 v105, v105, s28, v161
	v_med3_f32 v109, v109, s28, v161
	v_med3_f32 v113, v113, s28, v161
	v_med3_f32 v117, v117, s28, v161
	v_med3_f32 v121, v121, s28, v161
	v_med3_f32 v125, v125, s28, v161
	v_cvt_pk_fp8_f32 v152, v65, v69
	v_cvt_pk_fp8_f32 v153, v81, v85
	v_cvt_pk_fp8_f32 v154, v97, v101
	v_cvt_pk_fp8_f32 v155, v113, v117
	v_cvt_pk_fp8_f32 v152, v73, v77 op_sel:[0,0,1]
	v_cvt_pk_fp8_f32 v153, v89, v93 op_sel:[0,0,1]
	v_cvt_pk_fp8_f32 v154, v105, v109 op_sel:[0,0,1]
	v_cvt_pk_fp8_f32 v155, v121, v125 op_sel:[0,0,1]
	s_nop 0
	global_store_dwordx4 v160, v[152:155], s[20:21] offset:1024
	v_mul_f32_e32 v66, 0x42000000, v66
	v_mul_f32_e32 v70, 0x42000000, v70
	v_mul_f32_e32 v74, 0x42000000, v74
	v_mul_f32_e32 v78, 0x42000000, v78
	v_mul_f32_e32 v82, 0x42000000, v82
	v_mul_f32_e32 v86, 0x42000000, v86
	v_mul_f32_e32 v90, 0x42000000, v90
	v_mul_f32_e32 v94, 0x42000000, v94
	v_mul_f32_e32 v98, 0x42000000, v98
	v_mul_f32_e32 v102, 0x42000000, v102
	v_mul_f32_e32 v106, 0x42000000, v106
	v_mul_f32_e32 v110, 0x42000000, v110
	v_mul_f32_e32 v114, 0x42000000, v114
	v_mul_f32_e32 v118, 0x42000000, v118
	v_mul_f32_e32 v122, 0x42000000, v122
	v_mul_f32_e32 v126, 0x42000000, v126
	v_med3_f32 v66, v66, s28, v161
	v_med3_f32 v70, v70, s28, v161
	v_med3_f32 v74, v74, s28, v161
	v_med3_f32 v78, v78, s28, v161
	v_med3_f32 v82, v82, s28, v161
	v_med3_f32 v86, v86, s28, v161
	v_med3_f32 v90, v90, s28, v161
	v_med3_f32 v94, v94, s28, v161
	v_med3_f32 v98, v98, s28, v161
	v_med3_f32 v102, v102, s28, v161
	v_med3_f32 v106, v106, s28, v161
	v_med3_f32 v110, v110, s28, v161
	v_med3_f32 v114, v114, s28, v161
	v_med3_f32 v118, v118, s28, v161
	v_med3_f32 v122, v122, s28, v161
	v_med3_f32 v126, v126, s28, v161
	v_cvt_pk_fp8_f32 v148, v66, v70
	v_cvt_pk_fp8_f32 v149, v82, v86
	v_cvt_pk_fp8_f32 v150, v98, v102
	v_cvt_pk_fp8_f32 v151, v114, v118
	v_cvt_pk_fp8_f32 v148, v74, v78 op_sel:[0,0,1]
	v_cvt_pk_fp8_f32 v149, v90, v94 op_sel:[0,0,1]
	v_cvt_pk_fp8_f32 v150, v106, v110 op_sel:[0,0,1]
	v_cvt_pk_fp8_f32 v151, v122, v126 op_sel:[0,0,1]
	s_nop 0
	global_store_dwordx4 v160, v[148:151], s[20:21] offset:2048
	v_mul_f32_e32 v67, 0x42000000, v67
	v_mul_f32_e32 v71, 0x42000000, v71
	v_mul_f32_e32 v75, 0x42000000, v75
	v_mul_f32_e32 v79, 0x42000000, v79
	v_mul_f32_e32 v83, 0x42000000, v83
	v_mul_f32_e32 v87, 0x42000000, v87
	v_mul_f32_e32 v91, 0x42000000, v91
	v_mul_f32_e32 v95, 0x42000000, v95
	v_mul_f32_e32 v99, 0x42000000, v99
	v_mul_f32_e32 v103, 0x42000000, v103
	v_mul_f32_e32 v107, 0x42000000, v107
	v_mul_f32_e32 v111, 0x42000000, v111
	v_mul_f32_e32 v115, 0x42000000, v115
	v_mul_f32_e32 v119, 0x42000000, v119
	v_mul_f32_e32 v123, 0x42000000, v123
	v_mul_f32_e32 v127, 0x42000000, v127
	v_med3_f32 v67, v67, s28, v161
	v_med3_f32 v71, v71, s28, v161
	v_med3_f32 v75, v75, s28, v161
	v_med3_f32 v79, v79, s28, v161
	v_med3_f32 v83, v83, s28, v161
	v_med3_f32 v87, v87, s28, v161
	v_med3_f32 v91, v91, s28, v161
	v_med3_f32 v95, v95, s28, v161
	v_med3_f32 v99, v99, s28, v161
	v_med3_f32 v103, v103, s28, v161
	v_med3_f32 v107, v107, s28, v161
	v_med3_f32 v111, v111, s28, v161
	v_med3_f32 v115, v115, s28, v161
	v_med3_f32 v119, v119, s28, v161
	v_med3_f32 v123, v123, s28, v161
	v_med3_f32 v127, v127, s28, v161
	v_cvt_pk_fp8_f32 v152, v67, v71
	v_cvt_pk_fp8_f32 v153, v83, v87
	v_cvt_pk_fp8_f32 v154, v99, v103
	v_cvt_pk_fp8_f32 v155, v115, v119
	v_cvt_pk_fp8_f32 v152, v75, v79 op_sel:[0,0,1]
	v_cvt_pk_fp8_f32 v153, v91, v95 op_sel:[0,0,1]
	v_cvt_pk_fp8_f32 v154, v107, v111 op_sel:[0,0,1]
	v_cvt_pk_fp8_f32 v155, v123, v127 op_sel:[0,0,1]
	s_nop 0
	global_store_dwordx4 v160, v[152:155], s[20:21] offset:3072
	s_cmp_ge_u32 s7, s6
	s_cbranch_scc1 .Lp9c0_done
	s_mov_b32 s4, s7
	s_add_i32 s7, s4, s5
	s_cmp_lt_u32 s7, s6
	s_cbranch_scc0 .Lp9c0_A_last
	s_lshr_b32 s22, s7, 8
	s_and_b32 s23, s7, 0xff
	s_and_b32 s27, s22, 1
	s_lshr_b32 s22, s22, 1
	s_cmp_eq_u32 s27, 0
	s_cselect_b64 s[16:17], s[12:13], s[14:15]
	s_add_i32 s22, s22, 40
	s_lshl_b32 s24, s22, 22
	s_lshr_b32 s25, s23, 5
	s_lshl_b32 s25, s25, 19
	s_and_b32 s26, s23, 31
	s_lshl_b32 s26, s26, 7
	s_add_i32 s24, s24, s25
	s_add_i32 s24, s24, s26
	s_add_u32 s16, s16, s24
	s_addc_u32 s17, s17, 0
	s_nop 0
	global_load_dwordx4 v[64:67], v156, s[16:17] nt
	global_load_dwordx4 v[68:71], v157, s[16:17] nt
	global_load_dwordx4 v[72:75], v158, s[16:17] nt
	global_load_dwordx4 v[76:79], v159, s[16:17] nt
	s_add_u32 s16, s16, 0x4000
	s_addc_u32 s17, s17, 0
	s_nop 0
	global_load_dwordx4 v[80:83], v156, s[16:17] nt
	global_load_dwordx4 v[84:87], v157, s[16:17] nt
	global_load_dwordx4 v[88:91], v158, s[16:17] nt
	global_load_dwordx4 v[92:95], v159, s[16:17] nt
	s_add_u32 s16, s16, 0x4000
	s_addc_u32 s17, s17, 0
	s_nop 0
	global_load_dwordx4 v[96:99], v156, s[16:17] nt
	global_load_dwordx4 v[100:103], v157, s[16:17] nt
	global_load_dwordx4 v[104:107], v158, s[16:17] nt
	global_load_dwordx4 v[108:111], v159, s[16:17] nt
	s_add_u32 s16, s16, 0x4000
	s_addc_u32 s17, s17, 0
	s_nop 0
	global_load_dwordx4 v[112:115], v156, s[16:17] nt
	global_load_dwordx4 v[116:119], v157, s[16:17] nt
	global_load_dwordx4 v[120:123], v158, s[16:17] nt
	global_load_dwordx4 v[124:127], v159, s[16:17] nt
	s_waitcnt vmcnt(20)
	s_branch .Lp9c0_A_st

.Lp9c0_A_st:
	s_lshr_b32 s22, s4, 8
	s_and_b32 s23, s4, 0xff
	s_and_b32 s27, s22, 1
	s_lshr_b32 s22, s22, 1
	s_add_i32 s22, s22, 40
	s_mul_i32 s24, s22, 0x300000
	s_lshr_b32 s25, s23, 5
	s_lshl_b32 s25, s25, 7
	s_add_i32 s24, s24, s25
	s_and_b32 s26, s23, 31
	s_lshr_b32 s25, s26, 2
	s_lshl_b32 s25, s25, 18
	s_add_i32 s24, s24, s25
	s_lshl_b32 s25, s27, 17
	s_add_i32 s24, s24, s25
	s_and_b32 s25, s26, 3
	s_lshl_b32 s25, s25, 15
	s_add_i32 s24, s24, s25
	s_add_u32 s20, s10, s24
	s_addc_u32 s21, s11, 0
	v_mul_f32_e32 v0, 0x42000000, v0
	v_mul_f32_e32 v4, 0x42000000, v4
	v_mul_f32_e32 v8, 0x42000000, v8
	v_mul_f32_e32 v12, 0x42000000, v12
	v_mul_f32_e32 v16, 0x42000000, v16
	v_mul_f32_e32 v20, 0x42000000, v20
	v_mul_f32_e32 v24, 0x42000000, v24
	v_mul_f32_e32 v28, 0x42000000, v28
	v_mul_f32_e32 v32, 0x42000000, v32
	v_mul_f32_e32 v36, 0x42000000, v36
	v_mul_f32_e32 v40, 0x42000000, v40
	v_mul_f32_e32 v44, 0x42000000, v44
	v_mul_f32_e32 v48, 0x42000000, v48
	v_mul_f32_e32 v52, 0x42000000, v52
	v_mul_f32_e32 v56, 0x42000000, v56
	v_mul_f32_e32 v60, 0x42000000, v60
	v_med3_f32 v0, v0, s28, v161
	v_med3_f32 v4, v4, s28, v161
	v_med3_f32 v8, v8, s28, v161
	v_med3_f32 v12, v12, s28, v161
	v_med3_f32 v16, v16, s28, v161
	v_med3_f32 v20, v20, s28, v161
	v_med3_f32 v24, v24, s28, v161
	v_med3_f32 v28, v28, s28, v161
	v_med3_f32 v32, v32, s28, v161
	v_med3_f32 v36, v36, s28, v161
	v_med3_f32 v40, v40, s28, v161
	v_med3_f32 v44, v44, s28, v161
	v_med3_f32 v48, v48, s28, v161
	v_med3_f32 v52, v52, s28, v161
	v_med3_f32 v56, v56, s28, v161
	v_med3_f32 v60, v60, s28, v161
	v_cvt_pk_fp8_f32 v148, v0, v4
	v_cvt_pk_fp8_f32 v149, v16, v20
	v_cvt_pk_fp8_f32 v150, v32, v36
	v_cvt_pk_fp8_f32 v151, v48, v52
	v_cvt_pk_fp8_f32 v148, v8, v12 op_sel:[0,0,1]
	v_cvt_pk_fp8_f32 v149, v24, v28 op_sel:[0,0,1]
	v_cvt_pk_fp8_f32 v150, v40, v44 op_sel:[0,0,1]
	v_cvt_pk_fp8_f32 v151, v56, v60 op_sel:[0,0,1]
	s_nop 0
	global_store_dwordx4 v160, v[148:151], s[20:21]
	v_mul_f32_e32 v1, 0x42000000, v1
	v_mul_f32_e32 v5, 0x42000000, v5
	v_mul_f32_e32 v9, 0x42000000, v9
	v_mul_f32_e32 v13, 0x42000000, v13
	v_mul_f32_e32 v17, 0x42000000, v17
	v_mul_f32_e32 v21, 0x42000000, v21
	v_mul_f32_e32 v25, 0x42000000, v25
	v_mul_f32_e32 v29, 0x42000000, v29
	v_mul_f32_e32 v33, 0x42000000, v33
	v_mul_f32_e32 v37, 0x42000000, v37
	v_mul_f32_e32 v41, 0x42000000, v41
	v_mul_f32_e32 v45, 0x42000000, v45
	v_mul_f32_e32 v49, 0x42000000, v49
	v_mul_f32_e32 v53, 0x42000000, v53
	v_mul_f32_e32 v57, 0x42000000, v57
	v_mul_f32_e32 v61, 0x42000000, v61
	v_med3_f32 v1, v1, s28, v161
	v_med3_f32 v5, v5, s28, v161
	v_med3_f32 v9, v9, s28, v161
	v_med3_f32 v13, v13, s28, v161
	v_med3_f32 v17, v17, s28, v161
	v_med3_f32 v21, v21, s28, v161
	v_med3_f32 v25, v25, s28, v161
	v_med3_f32 v29, v29, s28, v161
	v_med3_f32 v33, v33, s28, v161
	v_med3_f32 v37, v37, s28, v161
	v_med3_f32 v41, v41, s28, v161
	v_med3_f32 v45, v45, s28, v161
	v_med3_f32 v49, v49, s28, v161
	v_med3_f32 v53, v53, s28, v161
	v_med3_f32 v57, v57, s28, v161
	v_med3_f32 v61, v61, s28, v161
	v_cvt_pk_fp8_f32 v152, v1, v5
	v_cvt_pk_fp8_f32 v153, v17, v21
	v_cvt_pk_fp8_f32 v154, v33, v37
	v_cvt_pk_fp8_f32 v155, v49, v53
	v_cvt_pk_fp8_f32 v152, v9, v13 op_sel:[0,0,1]
	v_cvt_pk_fp8_f32 v153, v25, v29 op_sel:[0,0,1]
	v_cvt_pk_fp8_f32 v154, v41, v45 op_sel:[0,0,1]
	v_cvt_pk_fp8_f32 v155, v57, v61 op_sel:[0,0,1]
	s_nop 0
	global_store_dwordx4 v160, v[152:155], s[20:21] offset:1024
	v_mul_f32_e32 v2, 0x42000000, v2
	v_mul_f32_e32 v6, 0x42000000, v6
	v_mul_f32_e32 v10, 0x42000000, v10
	v_mul_f32_e32 v14, 0x42000000, v14
	v_mul_f32_e32 v18, 0x42000000, v18
	v_mul_f32_e32 v22, 0x42000000, v22
	v_mul_f32_e32 v26, 0x42000000, v26
	v_mul_f32_e32 v30, 0x42000000, v30
	v_mul_f32_e32 v34, 0x42000000, v34
	v_mul_f32_e32 v38, 0x42000000, v38
	v_mul_f32_e32 v42, 0x42000000, v42
	v_mul_f32_e32 v46, 0x42000000, v46
	v_mul_f32_e32 v50, 0x42000000, v50
	v_mul_f32_e32 v54, 0x42000000, v54
	v_mul_f32_e32 v58, 0x42000000, v58
	v_mul_f32_e32 v62, 0x42000000, v62
	v_med3_f32 v2, v2, s28, v161
	v_med3_f32 v6, v6, s28, v161
	v_med3_f32 v10, v10, s28, v161
	v_med3_f32 v14, v14, s28, v161
	v_med3_f32 v18, v18, s28, v161
	v_med3_f32 v22, v22, s28, v161
	v_med3_f32 v26, v26, s28, v161
	v_med3_f32 v30, v30, s28, v161
	v_med3_f32 v34, v34, s28, v161
	v_med3_f32 v38, v38, s28, v161
	v_med3_f32 v42, v42, s28, v161
	v_med3_f32 v46, v46, s28, v161
	v_med3_f32 v50, v50, s28, v161
	v_med3_f32 v54, v54, s28, v161
	v_med3_f32 v58, v58, s28, v161
	v_med3_f32 v62, v62, s28, v161
	v_cvt_pk_fp8_f32 v148, v2, v6
	v_cvt_pk_fp8_f32 v149, v18, v22
	v_cvt_pk_fp8_f32 v150, v34, v38
	v_cvt_pk_fp8_f32 v151, v50, v54
	v_cvt_pk_fp8_f32 v148, v10, v14 op_sel:[0,0,1]
	v_cvt_pk_fp8_f32 v149, v26, v30 op_sel:[0,0,1]
	v_cvt_pk_fp8_f32 v150, v42, v46 op_sel:[0,0,1]
	v_cvt_pk_fp8_f32 v151, v58, v62 op_sel:[0,0,1]
	s_nop 0
	global_store_dwordx4 v160, v[148:151], s[20:21] offset:2048
	v_mul_f32_e32 v3, 0x42000000, v3
	v_mul_f32_e32 v7, 0x42000000, v7
	v_mul_f32_e32 v11, 0x42000000, v11
	v_mul_f32_e32 v15, 0x42000000, v15
	v_mul_f32_e32 v19, 0x42000000, v19
	v_mul_f32_e32 v23, 0x42000000, v23
	v_mul_f32_e32 v27, 0x42000000, v27
	v_mul_f32_e32 v31, 0x42000000, v31
	v_mul_f32_e32 v35, 0x42000000, v35
	v_mul_f32_e32 v39, 0x42000000, v39
	v_mul_f32_e32 v43, 0x42000000, v43
	v_mul_f32_e32 v47, 0x42000000, v47
	v_mul_f32_e32 v51, 0x42000000, v51
	v_mul_f32_e32 v55, 0x42000000, v55
	v_mul_f32_e32 v59, 0x42000000, v59
	v_mul_f32_e32 v63, 0x42000000, v63
	v_med3_f32 v3, v3, s28, v161
	v_med3_f32 v7, v7, s28, v161
	v_med3_f32 v11, v11, s28, v161
	v_med3_f32 v15, v15, s28, v161
	v_med3_f32 v19, v19, s28, v161
	v_med3_f32 v23, v23, s28, v161
	v_med3_f32 v27, v27, s28, v161
	v_med3_f32 v31, v31, s28, v161
	v_med3_f32 v35, v35, s28, v161
	v_med3_f32 v39, v39, s28, v161
	v_med3_f32 v43, v43, s28, v161
	v_med3_f32 v47, v47, s28, v161
	v_med3_f32 v51, v51, s28, v161
	v_med3_f32 v55, v55, s28, v161
	v_med3_f32 v59, v59, s28, v161
	v_med3_f32 v63, v63, s28, v161
	v_cvt_pk_fp8_f32 v152, v3, v7
	v_cvt_pk_fp8_f32 v153, v19, v23
	v_cvt_pk_fp8_f32 v154, v35, v39
	v_cvt_pk_fp8_f32 v155, v51, v55
	v_cvt_pk_fp8_f32 v152, v11, v15 op_sel:[0,0,1]
	v_cvt_pk_fp8_f32 v153, v27, v31 op_sel:[0,0,1]
	v_cvt_pk_fp8_f32 v154, v43, v47 op_sel:[0,0,1]
	v_cvt_pk_fp8_f32 v155, v59, v63 op_sel:[0,0,1]
	s_nop 0
	global_store_dwordx4 v160, v[152:155], s[20:21] offset:3072
	s_cmp_ge_u32 s7, s6
	s_cbranch_scc1 .Lp9c0_done
	s_mov_b32 s4, s7
	s_branch .Lp9c0_loop
.Lp9c0_done:
	s_mov_b32 s4, s19
	s_mov_b32 s5, 0x160
	s_mov_b32 s6, 0x1c00
	s_waitcnt vmcnt(0)
	s_cmp_ge_u32 s4, s6
	s_cbranch_scc1 .Lp9c1_done
	v_readlane_b32 s8, v243, 7
	v_readlane_b32 s9, v243, 8
	s_load_dwordx2 s[10:11], s[8:9], 0x130
	s_load_dwordx2 s[12:13], s[8:9], 0xf8
	s_load_dwordx2 s[14:15], s[8:9], 0x108
	v_mbcnt_lo_u32_b32 v162, -1, 0
	v_mbcnt_hi_u32_b32 v162, -1, v162
	v_lshrrev_b32_e32 v163, 3, v162
	v_and_b32_e32 v162, 7, v162
	v_lshlrev_b32_e32 v156, 16, v163
	v_lshl_add_u32 v156, v162, 4, v156
	v_add_u32_e32 v157, 0x1000, v156
	v_add_u32_e32 v158, 0x2000, v156
	v_add_u32_e32 v159, 0x3000, v156
	v_lshlrev_b32_e32 v160, 12, v162
	v_lshl_add_u32 v160, v163, 4, v160
	v_mov_b32_e32 v161, 0x43e00000
	s_mov_b32 s28, 0xc3e00000
	s_waitcnt lgkmcnt(0)
	s_add_u32 s10, s10, 0x2900000
	s_addc_u32 s11, s11, 0
	s_lshr_b32 s22, s4, 8
	s_and_b32 s23, s4, 0xff
	s_and_b32 s27, s22, 1
	s_lshr_b32 s22, s22, 1
	s_cmp_eq_u32 s27, 0
	s_cselect_b64 s[16:17], s[12:13], s[14:15]
	s_add_i32 s22, s22, 50
	s_lshl_b32 s24, s22, 22
	s_lshr_b32 s25, s23, 5
	s_lshl_b32 s25, s25, 19
	s_and_b32 s26, s23, 31
	s_lshl_b32 s26, s26, 7
	s_add_i32 s24, s24, s25
	s_add_i32 s24, s24, s26
	s_add_u32 s16, s16, s24
	s_addc_u32 s17, s17, 0
	s_nop 0
	global_load_dwordx4 v[0:3], v156, s[16:17] nt
	global_load_dwordx4 v[4:7], v157, s[16:17] nt
	global_load_dwordx4 v[8:11], v158, s[16:17] nt
	global_load_dwordx4 v[12:15], v159, s[16:17] nt
	s_add_u32 s16, s16, 0x4000
	s_addc_u32 s17, s17, 0
	s_nop 0
	global_load_dwordx4 v[16:19], v156, s[16:17] nt
	global_load_dwordx4 v[20:23], v157, s[16:17] nt
	global_load_dwordx4 v[24:27], v158, s[16:17] nt
	global_load_dwordx4 v[28:31], v159, s[16:17] nt
	s_add_u32 s16, s16, 0x4000
	s_addc_u32 s17, s17, 0
	s_nop 0
	global_load_dwordx4 v[32:35], v156, s[16:17] nt
	global_load_dwordx4 v[36:39], v157, s[16:17] nt
	global_load_dwordx4 v[40:43], v158, s[16:17] nt
	global_load_dwordx4 v[44:47], v159, s[16:17] nt
	s_add_u32 s16, s16, 0x4000
	s_addc_u32 s17, s17, 0
	s_nop 0
	global_load_dwordx4 v[48:51], v156, s[16:17] nt
	global_load_dwordx4 v[52:55], v157, s[16:17] nt
	global_load_dwordx4 v[56:59], v158, s[16:17] nt
	global_load_dwordx4 v[60:63], v159, s[16:17] nt
	s_add_i32 s7, s4, s5
	s_cmp_lt_u32 s7, s6
	s_cbranch_scc0 .Lp9c1_p_last
	s_lshr_b32 s22, s7, 8
	s_and_b32 s23, s7, 0xff
	s_and_b32 s27, s22, 1
	s_lshr_b32 s22, s22, 1
	s_cmp_eq_u32 s27, 0
	s_cselect_b64 s[16:17], s[12:13], s[14:15]
	s_add_i32 s22, s22, 50
	s_lshl_b32 s24, s22, 22
	s_lshr_b32 s25, s23, 5
	s_lshl_b32 s25, s25, 19
	s_and_b32 s26, s23, 31
	s_lshl_b32 s26, s26, 7
	s_add_i32 s24, s24, s25
	s_add_i32 s24, s24, s26
	s_add_u32 s16, s16, s24
	s_addc_u32 s17, s17, 0
	s_nop 0
	global_load_dwordx4 v[64:67], v156, s[16:17] nt
	global_load_dwordx4 v[68:71], v157, s[16:17] nt
	global_load_dwordx4 v[72:75], v158, s[16:17] nt
	global_load_dwordx4 v[76:79], v159, s[16:17] nt
	s_add_u32 s16, s16, 0x4000
	s_addc_u32 s17, s17, 0
	s_nop 0
	global_load_dwordx4 v[80:83], v156, s[16:17] nt
	global_load_dwordx4 v[84:87], v157, s[16:17] nt
	global_load_dwordx4 v[88:91], v158, s[16:17] nt
	global_load_dwordx4 v[92:95], v159, s[16:17] nt
	s_add_u32 s16, s16, 0x4000
	s_addc_u32 s17, s17, 0
	s_nop 0
	global_load_dwordx4 v[96:99], v156, s[16:17] nt
	global_load_dwordx4 v[100:103], v157, s[16:17] nt
	global_load_dwordx4 v[104:107], v158, s[16:17] nt
	global_load_dwordx4 v[108:111], v159, s[16:17] nt
	s_add_u32 s16, s16, 0x4000
	s_addc_u32 s17, s17, 0
	s_nop 0
	global_load_dwordx4 v[112:115], v156, s[16:17] nt
	global_load_dwordx4 v[116:119], v157, s[16:17] nt
	global_load_dwordx4 v[120:123], v158, s[16:17] nt
	global_load_dwordx4 v[124:127], v159, s[16:17] nt
	s_waitcnt vmcnt(16)
	s_branch .Lp9c1_p_st
